# plus non-temporal: gate pre-activation stores in the input projection, attention Q fragment loads, scan end-state loads, adaLN weight loads
# baseline (speedup 1.0000x reference)
; #define LAS __attribute__((address_space(3)))
; DI void p_adaln_unit(Frame& F, int unit) {
;     ...
;     for (int k0 = 0; k0 < 128; k0 += 32) {
;         float wv[32];
; #pragma unroll
;         for (int kk = 0; kk < 32; ++kk) wv[kk] = wp[(size_t)(F.wave * 128 + k0 + kk) * (NMOD * D)];
; #pragma unroll
;         for (int kk = 0; kk < 32; ++kk) { const int k = F.wave * 128 + k0 + kk; const float w = wv[kk];
;             const LAS f32x4* cp = (const LAS f32x4*)(condT + k * 16);
; #pragma unroll
;             for (int q = 0; q < 4; ++q) { const f32x4 cv = cp[q]; acc[4 * q] += cv[0] * w; acc[4 * q + 1] += cv[1] * w; acc[4 * q + 2] += cv[2] * w; acc[4 * q + 3] += cv[3] * w; } } }
.LBB0_12:
	s_mov_b32 s10, 0xfff46000
	v_add_co_u32_e32 v26, vcc, s10, v4
	s_mov_b32 s10, 0xfff4c000
	s_nop 0
	v_addc_co_u32_e32 v27, vcc, -1, v5, vcc
	global_load_dword v8, v[26:27], off nt
	v_add_co_u32_e32 v26, vcc, s10, v4
	s_mov_b32 s10, 0xfff52000
	s_nop 0
	v_addc_co_u32_e32 v27, vcc, -1, v5, vcc
	global_load_dword v32, v[26:27], off nt
	v_add_co_u32_e32 v26, vcc, s10, v4
	s_mov_b32 s10, 0xfff58000
	s_nop 0
	v_addc_co_u32_e32 v27, vcc, -1, v5, vcc
	global_load_dword v36, v[26:27], off nt
	v_add_co_u32_e32 v26, vcc, s10, v4
	s_mov_b32 s10, 0xfff5e000
	s_nop 0
	v_addc_co_u32_e32 v27, vcc, -1, v5, vcc
	global_load_dword v42, v[26:27], off nt
	v_add_co_u32_e32 v26, vcc, s10, v4
	s_mov_b32 s10, 0xfff64000
	s_nop 0
	v_addc_co_u32_e32 v27, vcc, -1, v5, vcc
	global_load_dword v46, v[26:27], off nt
	v_add_co_u32_e32 v26, vcc, s10, v4
	s_mov_b32 s10, 0xfff6a000
	s_nop 0
	v_addc_co_u32_e32 v27, vcc, -1, v5, vcc
	global_load_dword v52, v[26:27], off nt
	v_add_co_u32_e32 v26, vcc, s10, v4
	s_mov_b32 s10, 0xfff70000
	s_nop 0
	v_addc_co_u32_e32 v27, vcc, -1, v5, vcc
	global_load_dword v56, v[26:27], off nt
	v_add_co_u32_e32 v26, vcc, s10, v4
	s_mov_b32 s10, 0xfff76000
	s_nop 0
	v_addc_co_u32_e32 v27, vcc, -1, v5, vcc
	global_load_dword v62, v[26:27], off nt
	v_add_co_u32_e32 v26, vcc, s10, v4
	s_mov_b32 s10, 0xfff7c000
	s_nop 0
	v_addc_co_u32_e32 v27, vcc, -1, v5, vcc
	global_load_dword v66, v[26:27], off nt
	v_add_co_u32_e32 v26, vcc, s10, v4
	s_mov_b32 s10, 0xfff82000
	s_nop 0
	v_addc_co_u32_e32 v27, vcc, -1, v5, vcc
	global_load_dword v72, v[26:27], off nt
	v_add_co_u32_e32 v26, vcc, s10, v4
	s_mov_b32 s10, 0xfff88000
	s_nop 0
	v_addc_co_u32_e32 v27, vcc, -1, v5, vcc
	global_load_dword v24, v[26:27], off nt
	v_add_co_u32_e32 v26, vcc, s10, v4
	s_mov_b32 s10, 0xfff8e000
	s_nop 0
	v_addc_co_u32_e32 v27, vcc, -1, v5, vcc
	global_load_dword v28, v[26:27], off nt
	v_add_co_u32_e32 v26, vcc, s10, v4
	s_mov_b32 s10, 0xfff94000
	s_nop 0
	v_addc_co_u32_e32 v27, vcc, -1, v5, vcc
	global_load_dword v34, v[26:27], off nt
	v_add_co_u32_e32 v26, vcc, s10, v4
	s_mov_b32 s10, 0xfff9a000
	s_nop 0
	v_addc_co_u32_e32 v27, vcc, -1, v5, vcc
	global_load_dword v38, v[26:27], off nt
	v_add_co_u32_e32 v26, vcc, s10, v4
	s_mov_b32 s10, 0xfffa0000
	s_nop 0
	v_addc_co_u32_e32 v27, vcc, -1, v5, vcc
	global_load_dword v44, v[26:27], off nt
	v_add_co_u32_e32 v26, vcc, s10, v4
	s_mov_b32 s10, 0xfffa6000
	s_nop 0
	v_addc_co_u32_e32 v27, vcc, -1, v5, vcc
	global_load_dword v48, v[26:27], off nt
	v_add_co_u32_e32 v26, vcc, s10, v4
	s_mov_b32 s10, 0xfffac000
	s_nop 0
	v_addc_co_u32_e32 v27, vcc, -1, v5, vcc
	global_load_dword v54, v[26:27], off nt
	v_add_co_u32_e32 v26, vcc, s10, v4
	s_mov_b32 s10, 0xfffb2000
	s_nop 0
	v_addc_co_u32_e32 v27, vcc, -1, v5, vcc
	global_load_dword v58, v[26:27], off nt
	v_add_co_u32_e32 v26, vcc, s10, v4
	s_mov_b32 s10, 0xfffb8000
	s_nop 0
	v_addc_co_u32_e32 v27, vcc, -1, v5, vcc
	global_load_dword v64, v[26:27], off nt
	v_add_co_u32_e32 v26, vcc, s10, v4
	s_mov_b32 s10, 0xfffbe000
	s_nop 0
	v_addc_co_u32_e32 v27, vcc, -1, v5, vcc
	global_load_dword v68, v[26:27], off nt
	v_add_co_u32_e32 v26, vcc, s10, v4
	s_mov_b32 s10, 0xfffc4000
	s_nop 0
	v_addc_co_u32_e32 v27, vcc, -1, v5, vcc
	global_load_dword v76, v[26:27], off nt
	v_add_co_u32_e32 v26, vcc, s10, v4
	s_mov_b32 s10, 0xfffca000
	s_nop 0
	v_addc_co_u32_e32 v27, vcc, -1, v5, vcc
	v_add_co_u32_e32 v30, vcc, s10, v4
	s_mov_b32 s10, 0xfffd0000
	s_nop 0
	v_addc_co_u32_e32 v31, vcc, -1, v5, vcc
	v_add_co_u32_e32 v40, vcc, s10, v4
	s_mov_b32 s10, 0xfffd6000
	s_nop 0
	v_addc_co_u32_e32 v41, vcc, -1, v5, vcc
	global_load_dword v26, v[26:27], off nt
	v_mov_b32_e32 v1, s13
	global_load_dword v30, v[30:31], off nt
	s_add_i32 s14, s14, 32
	global_load_dword v31, v[40:41], off nt
	v_add_co_u32_e32 v40, vcc, s10, v4
	s_mov_b32 s10, 0xfffdc000
	s_nop 0
	v_addc_co_u32_e32 v41, vcc, -1, v5, vcc
	v_add_co_u32_e32 v50, vcc, s10, v4
	s_mov_b32 s10, 0xfffe2000
	s_nop 0
	v_addc_co_u32_e32 v51, vcc, -1, v5, vcc
	global_load_dword v40, v[40:41], off nt
	s_addk_i32 s13, 0x800
	global_load_dword v41, v[50:51], off nt
	v_add_co_u32_e32 v50, vcc, s10, v4
	s_mov_b32 s10, 0xfffe8000
	s_nop 0
	v_addc_co_u32_e32 v51, vcc, -1, v5, vcc
	v_add_co_u32_e32 v60, vcc, s10, v4
	s_mov_b32 s10, 0xfffee000
	s_nop 0
	v_addc_co_u32_e32 v61, vcc, -1, v5, vcc
	global_load_dword v50, v[50:51], off nt
	s_cmpk_gt_u32 s14, 0x5f
	global_load_dword v51, v[60:61], off nt
	v_add_co_u32_e32 v60, vcc, s10, v4
	s_mov_b32 s10, 0xffff4000
	s_nop 0
	v_addc_co_u32_e32 v61, vcc, -1, v5, vcc
	v_add_co_u32_e32 v70, vcc, s10, v4
	s_movk_i32 s10, 0xa000
	s_nop 0
	v_addc_co_u32_e32 v71, vcc, -1, v5, vcc
	global_load_dword v60, v[60:61], off nt
	s_nop 0
	global_load_dword v61, v[70:71], off nt
	v_add_co_u32_e32 v70, vcc, s10, v4
	s_mov_b64 s[10:11], 0xc0000
	s_nop 0
	v_addc_co_u32_e32 v71, vcc, -1, v5, vcc
	global_load_dword v70, v[70:71], off nt
	s_nop 0
	global_load_dword v74, v[4:5], off nt
	ds_read_b128 v[78:81], v1
	ds_read_b128 v[82:85], v1 offset:16
	ds_read_b128 v[86:89], v1 offset:32
	ds_read_b128 v[90:93], v1 offset:48
	ds_read_b128 v[94:97], v1 offset:64
	ds_read_b128 v[98:101], v1 offset:80
	ds_read_b128 v[102:105], v1 offset:96
	ds_read_b128 v[106:109], v1 offset:112
	ds_read_b128 v[110:113], v1 offset:128
	ds_read_b128 v[114:117], v1 offset:144
	ds_read_b128 v[118:121], v1 offset:160
	ds_read_b128 v[122:125], v1 offset:176
	ds_read_b128 v[126:129], v1 offset:192
	ds_read_b128 v[130:133], v1 offset:208
	ds_read_b128 v[134:137], v1 offset:224
	ds_read_b128 v[138:141], v1 offset:240
	ds_read_b128 v[142:145], v1 offset:256
	ds_read_b128 v[146:149], v1 offset:272
	ds_read_b128 v[150:153], v1 offset:288
	ds_read_b128 v[154:157], v1 offset:304
	ds_read_b128 v[158:161], v1 offset:320
	ds_read_b128 v[162:165], v1 offset:336
	ds_read_b128 v[166:169], v1 offset:352
	ds_read_b128 v[170:173], v1 offset:368
	ds_read_b128 v[174:177], v1 offset:384
	ds_read_b128 v[178:181], v1 offset:400
	ds_read_b128 v[182:185], v1 offset:416
	ds_read_b128 v[186:189], v1 offset:432
	ds_read_b128 v[190:193], v1 offset:448
	ds_read_b128 v[194:197], v1 offset:464
	ds_read_b128 v[198:201], v1 offset:480
	ds_read_b128 v[202:205], v1 offset:496
	ds_read_b128 v[206:209], v1 offset:512
	ds_read_b128 v[210:213], v1 offset:528
	ds_read_b128 v[214:217], v1 offset:544
	ds_read_b128 v[218:221], v1 offset:560
	ds_read_b128 v[222:225], v1 offset:576
	s_waitcnt vmcnt(31) lgkmcnt(14)
; #define LAS __attribute__((address_space(3)))
; DI void p_adaln_unit(Frame& F, int unit) {
;     ...
;         for (int kk = 0; kk < 32; ++kk) { const int k = F.wave * 128 + k0 + kk; const float w = wv[kk];
;             const LAS f32x4* cp = (const LAS f32x4*)(condT + k * 16);
; #pragma unroll
;             for (int q = 0; q < 4; ++q) { const f32x4 cv = cp[q]; acc[4 * q] += cv[0] * w; acc[4 * q + 1] += cv[1] * w; acc[4 * q + 2] += cv[2] * w; acc[4 * q + 3] += cv[3] * w; } } }
	v_pk_fma_f32 v[10:11], v[8:9], v[80:81], v[10:11] op_sel_hi:[0,1,1]
	s_waitcnt vmcnt(30)
	v_pk_fma_f32 v[10:11], v[32:33], v[96:97], v[10:11] op_sel_hi:[0,1,1]
	s_waitcnt vmcnt(29)
	v_pk_fma_f32 v[10:11], v[36:37], v[112:113], v[10:11] op_sel_hi:[0,1,1]
	s_waitcnt vmcnt(28)
	v_pk_fma_f32 v[10:11], v[42:43], v[128:129], v[10:11] op_sel_hi:[0,1,1]
	s_waitcnt vmcnt(27)
	v_pk_fma_f32 v[10:11], v[46:47], v[144:145], v[10:11] op_sel_hi:[0,1,1]
	s_waitcnt vmcnt(26)
	v_pk_fma_f32 v[10:11], v[52:53], v[160:161], v[10:11] op_sel_hi:[0,1,1]
	s_waitcnt vmcnt(25) lgkmcnt(12)
	v_pk_fma_f32 v[10:11], v[56:57], v[176:177], v[10:11] op_sel_hi:[0,1,1]
	s_waitcnt vmcnt(24) lgkmcnt(8)
	v_pk_fma_f32 v[10:11], v[62:63], v[192:193], v[10:11] op_sel_hi:[0,1,1]
	s_waitcnt vmcnt(23) lgkmcnt(4)
	v_pk_fma_f32 v[10:11], v[66:67], v[208:209], v[10:11] op_sel_hi:[0,1,1]
	s_waitcnt vmcnt(22) lgkmcnt(0)
	v_pk_fma_f32 v[230:231], v[72:73], v[224:225], v[10:11] op_sel_hi:[0,1,1]
	v_pk_fma_f32 v[10:11], v[8:9], v[82:83], v[12:13] op_sel_hi:[0,1,1]
	v_pk_fma_f32 v[10:11], v[32:33], v[98:99], v[10:11] op_sel_hi:[0,1,1]
	v_pk_fma_f32 v[10:11], v[36:37], v[114:115], v[10:11] op_sel_hi:[0,1,1]
	v_pk_fma_f32 v[10:11], v[42:43], v[130:131], v[10:11] op_sel_hi:[0,1,1]
	v_pk_fma_f32 v[6:7], v[8:9], v[78:79], v[6:7] op_sel_hi:[0,1,1]
	ds_read_b128 v[78:81], v1 offset:592
	v_pk_fma_f32 v[10:11], v[46:47], v[146:147], v[10:11] op_sel_hi:[0,1,1]
	v_pk_fma_f32 v[10:11], v[52:53], v[162:163], v[10:11] op_sel_hi:[0,1,1]
	v_pk_fma_f32 v[10:11], v[56:57], v[178:179], v[10:11] op_sel_hi:[0,1,1]
	v_pk_fma_f32 v[10:11], v[62:63], v[194:195], v[10:11] op_sel_hi:[0,1,1]
	v_pk_fma_f32 v[10:11], v[66:67], v[210:211], v[10:11] op_sel_hi:[0,1,1]
	s_waitcnt lgkmcnt(0)
	v_pk_fma_f32 v[232:233], v[72:73], v[78:79], v[10:11] op_sel_hi:[0,1,1]
	v_pk_fma_f32 v[10:11], v[8:9], v[84:85], v[14:15] op_sel_hi:[0,1,1]
	v_pk_fma_f32 v[10:11], v[32:33], v[100:101], v[10:11] op_sel_hi:[0,1,1]
	v_pk_fma_f32 v[10:11], v[36:37], v[116:117], v[10:11] op_sel_hi:[0,1,1]
	v_pk_fma_f32 v[10:11], v[42:43], v[132:133], v[10:11] op_sel_hi:[0,1,1]
	v_pk_fma_f32 v[10:11], v[46:47], v[148:149], v[10:11] op_sel_hi:[0,1,1]
	v_pk_fma_f32 v[10:11], v[52:53], v[164:165], v[10:11] op_sel_hi:[0,1,1]
	v_pk_fma_f32 v[14:15], v[8:9], v[86:87], v[16:17] op_sel_hi:[0,1,1]
	v_pk_fma_f32 v[10:11], v[56:57], v[180:181], v[10:11] op_sel_hi:[0,1,1]
	v_pk_fma_f32 v[14:15], v[32:33], v[102:103], v[14:15] op_sel_hi:[0,1,1]
	v_pk_fma_f32 v[10:11], v[62:63], v[196:197], v[10:11] op_sel_hi:[0,1,1]
	v_pk_fma_f32 v[14:15], v[36:37], v[118:119], v[14:15] op_sel_hi:[0,1,1]
	v_pk_fma_f32 v[10:11], v[66:67], v[212:213], v[10:11] op_sel_hi:[0,1,1]
	v_pk_fma_f32 v[14:15], v[42:43], v[134:135], v[14:15] op_sel_hi:[0,1,1]
	v_pk_fma_f32 v[234:235], v[72:73], v[80:81], v[10:11] op_sel_hi:[0,1,1]
	ds_read_b128 v[10:13], v1 offset:608
	v_pk_fma_f32 v[14:15], v[46:47], v[150:151], v[14:15] op_sel_hi:[0,1,1]
	v_pk_fma_f32 v[14:15], v[52:53], v[166:167], v[14:15] op_sel_hi:[0,1,1]
	v_pk_fma_f32 v[14:15], v[56:57], v[182:183], v[14:15] op_sel_hi:[0,1,1]
	v_pk_fma_f32 v[14:15], v[62:63], v[198:199], v[14:15] op_sel_hi:[0,1,1]
	v_pk_fma_f32 v[14:15], v[66:67], v[214:215], v[14:15] op_sel_hi:[0,1,1]
	s_waitcnt lgkmcnt(0)
	v_pk_fma_f32 v[236:237], v[72:73], v[10:11], v[14:15] op_sel_hi:[0,1,1]
	v_pk_fma_f32 v[10:11], v[8:9], v[88:89], v[20:21] op_sel_hi:[0,1,1]
	v_pk_fma_f32 v[10:11], v[32:33], v[104:105], v[10:11] op_sel_hi:[0,1,1]
	v_pk_fma_f32 v[10:11], v[36:37], v[120:121], v[10:11] op_sel_hi:[0,1,1]
	v_pk_fma_f32 v[10:11], v[42:43], v[136:137], v[10:11] op_sel_hi:[0,1,1]
	v_pk_fma_f32 v[10:11], v[46:47], v[152:153], v[10:11] op_sel_hi:[0,1,1]
	v_pk_fma_f32 v[10:11], v[52:53], v[168:169], v[10:11] op_sel_hi:[0,1,1]
	v_pk_fma_f32 v[14:15], v[8:9], v[90:91], v[22:23] op_sel_hi:[0,1,1]
	v_pk_fma_f32 v[10:11], v[56:57], v[184:185], v[10:11] op_sel_hi:[0,1,1]
	v_pk_fma_f32 v[14:15], v[32:33], v[106:107], v[14:15] op_sel_hi:[0,1,1]
	v_pk_fma_f32 v[10:11], v[62:63], v[200:201], v[10:11] op_sel_hi:[0,1,1]
	v_pk_fma_f32 v[14:15], v[36:37], v[122:123], v[14:15] op_sel_hi:[0,1,1]
	v_pk_fma_f32 v[10:11], v[66:67], v[216:217], v[10:11] op_sel_hi:[0,1,1]
	v_pk_fma_f32 v[14:15], v[42:43], v[138:139], v[14:15] op_sel_hi:[0,1,1]
	v_pk_fma_f32 v[238:239], v[72:73], v[12:13], v[10:11] op_sel_hi:[0,1,1]
	ds_read_b128 v[10:13], v1 offset:624
	v_pk_fma_f32 v[14:15], v[46:47], v[154:155], v[14:15] op_sel_hi:[0,1,1]
	v_pk_fma_f32 v[14:15], v[52:53], v[170:171], v[14:15] op_sel_hi:[0,1,1]
	v_pk_fma_f32 v[14:15], v[56:57], v[186:187], v[14:15] op_sel_hi:[0,1,1]
	v_pk_fma_f32 v[14:15], v[62:63], v[202:203], v[14:15] op_sel_hi:[0,1,1]
	v_pk_fma_f32 v[14:15], v[66:67], v[218:219], v[14:15] op_sel_hi:[0,1,1]
	s_waitcnt lgkmcnt(0)
; #define LAS __attribute__((address_space(3)))
; DI void p_adaln_unit(Frame& F, int unit) {
;     ...
;         for (int kk = 0; kk < 32; ++kk) { const int k = F.wave * 128 + k0 + kk; const float w = wv[kk];
;             const LAS f32x4* cp = (const LAS f32x4*)(condT + k * 16);
; #pragma unroll
;             for (int q = 0; q < 4; ++q) { const f32x4 cv = cp[q]; acc[4 * q] += cv[0] * w; acc[4 * q + 1] += cv[1] * w; acc[4 * q + 2] += cv[2] * w; acc[4 * q + 3] += cv[3] * w; } } }
	v_pk_fma_f32 v[22:23], v[72:73], v[10:11], v[14:15] op_sel_hi:[0,1,1]
	v_pk_fma_f32 v[10:11], v[8:9], v[92:93], v[18:19] op_sel_hi:[0,1,1]
	v_pk_fma_f32 v[6:7], v[32:33], v[94:95], v[6:7] op_sel_hi:[0,1,1]
	v_pk_fma_f32 v[10:11], v[32:33], v[108:109], v[10:11] op_sel_hi:[0,1,1]
	v_pk_fma_f32 v[6:7], v[36:37], v[110:111], v[6:7] op_sel_hi:[0,1,1]
	v_pk_fma_f32 v[10:11], v[36:37], v[124:125], v[10:11] op_sel_hi:[0,1,1]
	v_pk_fma_f32 v[6:7], v[42:43], v[126:127], v[6:7] op_sel_hi:[0,1,1]
	v_pk_fma_f32 v[10:11], v[42:43], v[140:141], v[10:11] op_sel_hi:[0,1,1]
	v_pk_fma_f32 v[6:7], v[46:47], v[142:143], v[6:7] op_sel_hi:[0,1,1]
	v_pk_fma_f32 v[10:11], v[46:47], v[156:157], v[10:11] op_sel_hi:[0,1,1]
	v_pk_fma_f32 v[6:7], v[52:53], v[158:159], v[6:7] op_sel_hi:[0,1,1]
	v_pk_fma_f32 v[10:11], v[52:53], v[172:173], v[10:11] op_sel_hi:[0,1,1]
	v_pk_fma_f32 v[6:7], v[56:57], v[174:175], v[6:7] op_sel_hi:[0,1,1]
	v_pk_fma_f32 v[10:11], v[56:57], v[188:189], v[10:11] op_sel_hi:[0,1,1]
	v_pk_fma_f32 v[6:7], v[62:63], v[190:191], v[6:7] op_sel_hi:[0,1,1]
	v_pk_fma_f32 v[10:11], v[62:63], v[204:205], v[10:11] op_sel_hi:[0,1,1]
	v_pk_fma_f32 v[6:7], v[66:67], v[206:207], v[6:7] op_sel_hi:[0,1,1]
	v_pk_fma_f32 v[10:11], v[66:67], v[220:221], v[10:11] op_sel_hi:[0,1,1]
	v_pk_fma_f32 v[6:7], v[72:73], v[222:223], v[6:7] op_sel_hi:[0,1,1]
	v_pk_fma_f32 v[32:33], v[72:73], v[12:13], v[10:11] op_sel_hi:[0,1,1]
	ds_read_b128 v[10:13], v1 offset:640
	ds_read_b128 v[14:17], v1 offset:656
	ds_read_b128 v[18:21], v1 offset:672
	ds_read_b128 v[78:81], v1 offset:688
	ds_read_b128 v[82:85], v1 offset:704
	ds_read_b128 v[86:89], v1 offset:720
	ds_read_b128 v[90:93], v1 offset:736
	ds_read_b128 v[94:97], v1 offset:752
	ds_read_b128 v[98:101], v1 offset:768
	ds_read_b128 v[102:105], v1 offset:784
	ds_read_b128 v[106:109], v1 offset:800
	ds_read_b128 v[110:113], v1 offset:816
	ds_read_b128 v[114:117], v1 offset:832
	ds_read_b128 v[118:121], v1 offset:848
	ds_read_b128 v[122:125], v1 offset:864
	ds_read_b128 v[126:129], v1 offset:880
	ds_read_b128 v[130:133], v1 offset:896
	ds_read_b128 v[134:137], v1 offset:912
	ds_read_b128 v[138:141], v1 offset:928
	ds_read_b128 v[142:145], v1 offset:944
	ds_read_b128 v[146:149], v1 offset:960
	ds_read_b128 v[150:153], v1 offset:976
	ds_read_b128 v[154:157], v1 offset:992
	ds_read_b128 v[158:161], v1 offset:1008
	ds_read_b128 v[162:165], v1 offset:1024
	ds_read_b128 v[166:169], v1 offset:1040
	ds_read_b128 v[170:173], v1 offset:1056
	ds_read_b128 v[174:177], v1 offset:1072
	ds_read_b128 v[178:181], v1 offset:1088
	ds_read_b128 v[182:185], v1 offset:1104
	ds_read_b128 v[186:189], v1 offset:1120
	ds_read_b128 v[190:193], v1 offset:1136
	ds_read_b128 v[194:197], v1 offset:1152
	ds_read_b128 v[198:201], v1 offset:1168
	ds_read_b128 v[202:205], v1 offset:1184
	ds_read_b128 v[206:209], v1 offset:1200
	ds_read_b128 v[210:213], v1 offset:1216
	ds_read_b128 v[214:217], v1 offset:1232
	ds_read_b128 v[218:221], v1 offset:1248
	ds_read_b128 v[222:225], v1 offset:1264
	ds_read_b128 v[226:229], v1 offset:1280
	s_waitcnt vmcnt(21) lgkmcnt(14)
	v_pk_fma_f32 v[6:7], v[24:25], v[10:11], v[6:7] op_sel_hi:[0,1,1]
	v_pk_fma_f32 v[10:11], v[24:25], v[12:13], v[230:231] op_sel_hi:[0,1,1]
	s_waitcnt vmcnt(20)
	v_pk_fma_f32 v[10:11], v[28:29], v[84:85], v[10:11] op_sel_hi:[0,1,1]
	s_waitcnt vmcnt(19)
	v_pk_fma_f32 v[10:11], v[34:35], v[100:101], v[10:11] op_sel_hi:[0,1,1]
	s_waitcnt vmcnt(18)
	v_pk_fma_f32 v[10:11], v[38:39], v[116:117], v[10:11] op_sel_hi:[0,1,1]
	s_waitcnt vmcnt(17)
	v_pk_fma_f32 v[10:11], v[44:45], v[132:133], v[10:11] op_sel_hi:[0,1,1]
	s_waitcnt vmcnt(16)
	v_pk_fma_f32 v[10:11], v[48:49], v[148:149], v[10:11] op_sel_hi:[0,1,1]
	v_pk_fma_f32 v[14:15], v[24:25], v[14:15], v[232:233] op_sel_hi:[0,1,1]
	s_waitcnt vmcnt(15)
	v_pk_fma_f32 v[10:11], v[54:55], v[164:165], v[10:11] op_sel_hi:[0,1,1]
	v_pk_fma_f32 v[14:15], v[28:29], v[86:87], v[14:15] op_sel_hi:[0,1,1]
	s_waitcnt vmcnt(14) lgkmcnt(12)
	v_pk_fma_f32 v[10:11], v[58:59], v[180:181], v[10:11] op_sel_hi:[0,1,1]
	v_pk_fma_f32 v[14:15], v[34:35], v[102:103], v[14:15] op_sel_hi:[0,1,1]
	v_pk_fma_f32 v[6:7], v[28:29], v[82:83], v[6:7] op_sel_hi:[0,1,1]
	s_waitcnt vmcnt(13) lgkmcnt(8)
	v_pk_fma_f32 v[10:11], v[64:65], v[196:197], v[10:11] op_sel_hi:[0,1,1]
	v_pk_fma_f32 v[14:15], v[38:39], v[118:119], v[14:15] op_sel_hi:[0,1,1]
	v_pk_fma_f32 v[6:7], v[34:35], v[98:99], v[6:7] op_sel_hi:[0,1,1]
	s_waitcnt vmcnt(12) lgkmcnt(4)
	v_pk_fma_f32 v[10:11], v[68:69], v[212:213], v[10:11] op_sel_hi:[0,1,1]
	v_pk_fma_f32 v[14:15], v[44:45], v[134:135], v[14:15] op_sel_hi:[0,1,1]
	v_pk_fma_f32 v[6:7], v[38:39], v[114:115], v[6:7] op_sel_hi:[0,1,1]
	s_waitcnt vmcnt(11) lgkmcnt(0)
	v_pk_fma_f32 v[72:73], v[76:77], v[228:229], v[10:11] op_sel_hi:[0,1,1]
	ds_read_b128 v[10:13], v1 offset:1296
	v_pk_fma_f32 v[14:15], v[48:49], v[150:151], v[14:15] op_sel_hi:[0,1,1]
	v_pk_fma_f32 v[6:7], v[44:45], v[130:131], v[6:7] op_sel_hi:[0,1,1]
	v_pk_fma_f32 v[14:15], v[54:55], v[166:167], v[14:15] op_sel_hi:[0,1,1]
	v_pk_fma_f32 v[6:7], v[48:49], v[146:147], v[6:7] op_sel_hi:[0,1,1]
	v_pk_fma_f32 v[14:15], v[58:59], v[182:183], v[14:15] op_sel_hi:[0,1,1]
	v_pk_fma_f32 v[6:7], v[54:55], v[162:163], v[6:7] op_sel_hi:[0,1,1]
	v_pk_fma_f32 v[14:15], v[64:65], v[198:199], v[14:15] op_sel_hi:[0,1,1]
	v_pk_fma_f32 v[6:7], v[58:59], v[178:179], v[6:7] op_sel_hi:[0,1,1]
	v_pk_fma_f32 v[14:15], v[68:69], v[214:215], v[14:15] op_sel_hi:[0,1,1]
	v_pk_fma_f32 v[6:7], v[64:65], v[194:195], v[6:7] op_sel_hi:[0,1,1]
	s_waitcnt lgkmcnt(0)
; #define LAS __attribute__((address_space(3)))
; DI void p_adaln_unit(Frame& F, int unit) {
;     ...
;         for (int kk = 0; kk < 32; ++kk) { const int k = F.wave * 128 + k0 + kk; const float w = wv[kk];
;             const LAS f32x4* cp = (const LAS f32x4*)(condT + k * 16);
; #pragma unroll
;             for (int q = 0; q < 4; ++q) { const f32x4 cv = cp[q]; acc[4 * q] += cv[0] * w; acc[4 * q + 1] += cv[1] * w; acc[4 * q + 2] += cv[2] * w; acc[4 * q + 3] += cv[3] * w; } } }
	v_pk_fma_f32 v[194:195], v[76:77], v[10:11], v[14:15] op_sel_hi:[0,1,1]
	v_pk_fma_f32 v[10:11], v[24:25], v[16:17], v[234:235] op_sel_hi:[0,1,1]
	v_pk_fma_f32 v[10:11], v[28:29], v[88:89], v[10:11] op_sel_hi:[0,1,1]
	v_pk_fma_f32 v[10:11], v[34:35], v[104:105], v[10:11] op_sel_hi:[0,1,1]
	v_pk_fma_f32 v[10:11], v[38:39], v[120:121], v[10:11] op_sel_hi:[0,1,1]
	v_pk_fma_f32 v[10:11], v[44:45], v[136:137], v[10:11] op_sel_hi:[0,1,1]
	v_pk_fma_f32 v[10:11], v[48:49], v[152:153], v[10:11] op_sel_hi:[0,1,1]
	v_pk_fma_f32 v[14:15], v[24:25], v[18:19], v[236:237] op_sel_hi:[0,1,1]
	v_pk_fma_f32 v[10:11], v[54:55], v[168:169], v[10:11] op_sel_hi:[0,1,1]
	v_pk_fma_f32 v[14:15], v[28:29], v[90:91], v[14:15] op_sel_hi:[0,1,1]
	v_pk_fma_f32 v[10:11], v[58:59], v[184:185], v[10:11] op_sel_hi:[0,1,1]
	v_pk_fma_f32 v[14:15], v[34:35], v[106:107], v[14:15] op_sel_hi:[0,1,1]
	v_pk_fma_f32 v[10:11], v[64:65], v[200:201], v[10:11] op_sel_hi:[0,1,1]
	v_pk_fma_f32 v[14:15], v[38:39], v[122:123], v[14:15] op_sel_hi:[0,1,1]
	v_pk_fma_f32 v[10:11], v[68:69], v[216:217], v[10:11] op_sel_hi:[0,1,1]
	v_pk_fma_f32 v[14:15], v[44:45], v[138:139], v[14:15] op_sel_hi:[0,1,1]
	v_pk_fma_f32 v[196:197], v[76:77], v[12:13], v[10:11] op_sel_hi:[0,1,1]
	ds_read_b128 v[10:13], v1 offset:1312
	v_pk_fma_f32 v[14:15], v[48:49], v[154:155], v[14:15] op_sel_hi:[0,1,1]
	v_pk_fma_f32 v[14:15], v[54:55], v[170:171], v[14:15] op_sel_hi:[0,1,1]
	v_pk_fma_f32 v[14:15], v[58:59], v[186:187], v[14:15] op_sel_hi:[0,1,1]
	v_pk_fma_f32 v[14:15], v[64:65], v[202:203], v[14:15] op_sel_hi:[0,1,1]
	v_pk_fma_f32 v[14:15], v[68:69], v[218:219], v[14:15] op_sel_hi:[0,1,1]
	s_waitcnt lgkmcnt(0)
	v_pk_fma_f32 v[198:199], v[76:77], v[10:11], v[14:15] op_sel_hi:[0,1,1]
	v_pk_fma_f32 v[10:11], v[24:25], v[20:21], v[238:239] op_sel_hi:[0,1,1]
	v_pk_fma_f32 v[10:11], v[28:29], v[92:93], v[10:11] op_sel_hi:[0,1,1]
	v_pk_fma_f32 v[10:11], v[34:35], v[108:109], v[10:11] op_sel_hi:[0,1,1]
	v_pk_fma_f32 v[10:11], v[38:39], v[124:125], v[10:11] op_sel_hi:[0,1,1]
	v_pk_fma_f32 v[10:11], v[44:45], v[140:141], v[10:11] op_sel_hi:[0,1,1]
	v_pk_fma_f32 v[10:11], v[48:49], v[156:157], v[10:11] op_sel_hi:[0,1,1]
	v_pk_fma_f32 v[14:15], v[24:25], v[78:79], v[22:23] op_sel_hi:[0,1,1]
	v_pk_fma_f32 v[10:11], v[54:55], v[172:173], v[10:11] op_sel_hi:[0,1,1]
	v_pk_fma_f32 v[14:15], v[28:29], v[94:95], v[14:15] op_sel_hi:[0,1,1]
	v_pk_fma_f32 v[10:11], v[58:59], v[188:189], v[10:11] op_sel_hi:[0,1,1]
	v_pk_fma_f32 v[14:15], v[34:35], v[110:111], v[14:15] op_sel_hi:[0,1,1]
	v_pk_fma_f32 v[10:11], v[64:65], v[204:205], v[10:11] op_sel_hi:[0,1,1]
	v_pk_fma_f32 v[14:15], v[38:39], v[126:127], v[14:15] op_sel_hi:[0,1,1]
	v_pk_fma_f32 v[10:11], v[68:69], v[220:221], v[10:11] op_sel_hi:[0,1,1]
	v_pk_fma_f32 v[14:15], v[44:45], v[142:143], v[14:15] op_sel_hi:[0,1,1]
	v_pk_fma_f32 v[200:201], v[76:77], v[12:13], v[10:11] op_sel_hi:[0,1,1]
	ds_read_b128 v[10:13], v1 offset:1328
	v_pk_fma_f32 v[14:15], v[48:49], v[158:159], v[14:15] op_sel_hi:[0,1,1]
	v_pk_fma_f32 v[14:15], v[54:55], v[174:175], v[14:15] op_sel_hi:[0,1,1]
	v_pk_fma_f32 v[14:15], v[58:59], v[190:191], v[14:15] op_sel_hi:[0,1,1]
	v_pk_fma_f32 v[14:15], v[64:65], v[206:207], v[14:15] op_sel_hi:[0,1,1]
	v_pk_fma_f32 v[14:15], v[68:69], v[222:223], v[14:15] op_sel_hi:[0,1,1]
	s_waitcnt lgkmcnt(0)
	v_pk_fma_f32 v[22:23], v[76:77], v[10:11], v[14:15] op_sel_hi:[0,1,1]
	ds_read_b128 v[14:17], v1 offset:1344
	ds_read_b128 v[18:21], v1 offset:1360
	ds_read_b128 v[82:85], v1 offset:1376
	ds_read_b128 v[86:89], v1 offset:1392
	v_mul_f32_e32 v10, v76, v12
	v_pk_fma_f32 v[6:7], v[68:69], v[210:211], v[6:7] op_sel_hi:[0,1,1]
	v_pk_fma_f32 v[6:7], v[76:77], v[226:227], v[6:7] op_sel_hi:[0,1,1]
	s_waitcnt vmcnt(10)
	v_mov_b32_e32 v77, v26
	s_waitcnt lgkmcnt(0)
	v_mul_f32_e32 v190, v26, v88
	v_mov_b32_e32 v88, v13
	v_pk_fma_f32 v[12:13], v[24:25], v[80:81], v[32:33] op_sel_hi:[0,1,1]
	v_pk_fma_f32 v[12:13], v[28:29], v[96:97], v[12:13] op_sel_hi:[0,1,1]
	v_pk_fma_f32 v[12:13], v[34:35], v[112:113], v[12:13] op_sel_hi:[0,1,1]
	v_pk_fma_f32 v[12:13], v[38:39], v[128:129], v[12:13] op_sel_hi:[0,1,1]
	v_pk_fma_f32 v[12:13], v[44:45], v[144:145], v[12:13] op_sel_hi:[0,1,1]
	v_pk_fma_f32 v[12:13], v[48:49], v[160:161], v[12:13] op_sel_hi:[0,1,1]
	v_pk_fma_f32 v[12:13], v[54:55], v[176:177], v[12:13] op_sel_hi:[0,1,1]
	v_pk_fma_f32 v[12:13], v[58:59], v[192:193], v[12:13] op_sel_hi:[0,1,1]
	v_pk_mul_f32 v[202:203], v[76:77], v[88:89]
	v_pk_fma_f32 v[12:13], v[64:65], v[208:209], v[12:13] op_sel_hi:[0,1,1]
	v_pk_fma_f32 v[12:13], v[68:69], v[224:225], v[12:13] op_sel_hi:[0,1,1]
	v_mov_b32_e32 v11, v202
	v_pk_add_f32 v[28:29], v[12:13], v[10:11]
	ds_read_b128 v[10:13], v1 offset:1408
	ds_read_b128 v[32:35], v1 offset:1424
	ds_read_b128 v[36:39], v1 offset:1440
	ds_read_b128 v[42:45], v1 offset:1456
	ds_read_b128 v[46:49], v1 offset:1472
	ds_read_b128 v[52:55], v1 offset:1488
	ds_read_b128 v[56:59], v1 offset:1504
	ds_read_b128 v[62:65], v1 offset:1520
	v_pk_fma_f32 v[6:7], v[26:27], v[14:15], v[6:7] op_sel_hi:[0,1,1]
	s_waitcnt vmcnt(8) lgkmcnt(7)
	v_pk_fma_f32 v[6:7], v[30:31], v[10:11], v[6:7] op_sel_hi:[0,1,1]
	v_pk_fma_f32 v[10:11], v[26:27], v[16:17], v[72:73] op_sel_hi:[0,1,1]
	v_pk_fma_f32 v[16:17], v[26:27], v[18:19], v[194:195] op_sel_hi:[0,1,1]
	s_waitcnt lgkmcnt(0)
	v_mul_f32_e32 v68, v31, v64
	v_mov_b32_e32 v64, v45
	v_pk_mul_f32 v[80:81], v[30:31], v[64:65]
	ds_read_b128 v[64:67], v1 offset:1536
	ds_read_b128 v[76:79], v1 offset:1552
	ds_read_b128 v[88:91], v1 offset:1568
	ds_read_b128 v[92:95], v1 offset:1584
	ds_read_b128 v[96:99], v1 offset:1600
	ds_read_b128 v[100:103], v1 offset:1616
	ds_read_b128 v[104:107], v1 offset:1632
	ds_read_b128 v[108:111], v1 offset:1648
	v_mov_b32_e32 v8, v31
	v_pk_fma_f32 v[16:17], v[30:31], v[32:33], v[16:17] op_sel_hi:[0,1,1]
	v_pk_fma_f32 v[16:17], v[8:9], v[52:53], v[16:17] op_sel_hi:[0,1,1]
	s_waitcnt vmcnt(6)
; #define LAS __attribute__((address_space(3)))
; DI void p_adaln_unit(Frame& F, int unit) {
;     ...
;         for (int kk = 0; kk < 32; ++kk) { const int k = F.wave * 128 + k0 + kk; const float w = wv[kk];
;             const LAS f32x4* cp = (const LAS f32x4*)(condT + k * 16);
; #pragma unroll
;             for (int q = 0; q < 4; ++q) { const f32x4 cv = cp[q]; acc[4 * q] += cv[0] * w; acc[4 * q + 1] += cv[1] * w; acc[4 * q + 2] += cv[2] * w; acc[4 * q + 3] += cv[3] * w; } } }
	v_mov_b32_e32 v24, v41
	s_waitcnt lgkmcnt(0)
	v_mul_f32_e32 v192, v41, v110
	v_mov_b32_e32 v110, v95
	v_pk_mul_f32 v[204:205], v[40:41], v[110:111]
	ds_read_b128 v[110:113], v1 offset:1664
	ds_read_b128 v[114:117], v1 offset:1680
	ds_read_b128 v[118:121], v1 offset:1696
	ds_read_b128 v[122:125], v1 offset:1712
	ds_read_b128 v[126:129], v1 offset:1728
	ds_read_b128 v[130:133], v1 offset:1744
	ds_read_b128 v[134:137], v1 offset:1760
	ds_read_b128 v[138:141], v1 offset:1776
	v_pk_fma_f32 v[16:17], v[40:41], v[76:77], v[16:17] op_sel_hi:[0,1,1]
	v_pk_fma_f32 v[16:17], v[24:25], v[100:101], v[16:17] op_sel_hi:[0,1,1]
	v_pk_fma_f32 v[6:7], v[8:9], v[46:47], v[6:7] op_sel_hi:[0,1,1]
	s_waitcnt vmcnt(4)
	v_mov_b32_e32 v46, v51
	s_waitcnt lgkmcnt(0)
	v_mul_f32_e32 v202, v51, v140
	v_mov_b32_e32 v140, v125
	v_pk_mul_f32 v[206:207], v[50:51], v[140:141]
	ds_read_b128 v[140:143], v1 offset:1792
	ds_read_b128 v[144:147], v1 offset:1808
	ds_read_b128 v[148:151], v1 offset:1824
	ds_read_b128 v[152:155], v1 offset:1840
	ds_read_b128 v[156:159], v1 offset:1856
	ds_read_b128 v[160:163], v1 offset:1872
	ds_read_b128 v[164:167], v1 offset:1888
	ds_read_b128 v[168:171], v1 offset:1904
	v_pk_fma_f32 v[10:11], v[30:31], v[12:13], v[10:11] op_sel_hi:[0,1,1]
	v_pk_fma_f32 v[16:17], v[50:51], v[114:115], v[16:17] op_sel_hi:[0,1,1]
	v_pk_fma_f32 v[16:17], v[46:47], v[130:131], v[16:17] op_sel_hi:[0,1,1]
	v_pk_fma_f32 v[6:7], v[40:41], v[64:65], v[6:7] op_sel_hi:[0,1,1]
	s_waitcnt vmcnt(2) lgkmcnt(0)
	v_mul_f32_e32 v208, v61, v170
	v_mov_b32_e32 v170, v155
	v_pk_mul_f32 v[210:211], v[60:61], v[170:171]
	ds_read_b128 v[170:173], v1 offset:1920
	ds_read_b128 v[174:177], v1 offset:1936
	ds_read_b128 v[178:181], v1 offset:1952
	ds_read_b128 v[182:185], v1 offset:1968
	ds_read_b128 v[186:189], v1 offset:1984
	ds_read_b128 v[12:15], v1 offset:2000
	v_mov_b32_e32 v64, v61
	v_pk_fma_f32 v[16:17], v[60:61], v[144:145], v[16:17] op_sel_hi:[0,1,1]
	v_pk_fma_f32 v[16:17], v[64:65], v[160:161], v[16:17] op_sel_hi:[0,1,1]
	s_waitcnt vmcnt(1) lgkmcnt(4)
	v_pk_fma_f32 v[16:17], v[70:71], v[174:175], v[16:17] op_sel_hi:[0,1,1]
	s_waitcnt vmcnt(0) lgkmcnt(0)
	v_pk_fma_f32 v[12:13], v[74:75], v[12:13], v[16:17] op_sel_hi:[0,1,1]
	v_pk_fma_f32 v[16:17], v[26:27], v[20:21], v[196:197] op_sel_hi:[0,1,1]
	v_pk_fma_f32 v[16:17], v[30:31], v[34:35], v[16:17] op_sel_hi:[0,1,1]
	v_pk_fma_f32 v[16:17], v[8:9], v[54:55], v[16:17] op_sel_hi:[0,1,1]
	v_pk_fma_f32 v[16:17], v[40:41], v[78:79], v[16:17] op_sel_hi:[0,1,1]
	v_pk_fma_f32 v[16:17], v[24:25], v[102:103], v[16:17] op_sel_hi:[0,1,1]
	v_pk_fma_f32 v[16:17], v[50:51], v[116:117], v[16:17] op_sel_hi:[0,1,1]
	v_pk_fma_f32 v[20:21], v[26:27], v[82:83], v[198:199] op_sel_hi:[0,1,1]
	v_pk_fma_f32 v[16:17], v[46:47], v[132:133], v[16:17] op_sel_hi:[0,1,1]
	v_pk_fma_f32 v[20:21], v[30:31], v[36:37], v[20:21] op_sel_hi:[0,1,1]
	v_pk_fma_f32 v[16:17], v[60:61], v[146:147], v[16:17] op_sel_hi:[0,1,1]
	v_pk_fma_f32 v[20:21], v[8:9], v[56:57], v[20:21] op_sel_hi:[0,1,1]
	v_pk_fma_f32 v[16:17], v[64:65], v[162:163], v[16:17] op_sel_hi:[0,1,1]
	v_pk_fma_f32 v[20:21], v[40:41], v[88:89], v[20:21] op_sel_hi:[0,1,1]
	v_pk_fma_f32 v[16:17], v[70:71], v[176:177], v[16:17] op_sel_hi:[0,1,1]
	v_pk_fma_f32 v[20:21], v[24:25], v[104:105], v[20:21] op_sel_hi:[0,1,1]
	v_pk_fma_f32 v[14:15], v[74:75], v[14:15], v[16:17] op_sel_hi:[0,1,1]
	ds_read_b128 v[16:19], v1 offset:2016
	ds_read_b128 v[32:35], v1 offset:2032
	v_pk_fma_f32 v[20:21], v[50:51], v[118:119], v[20:21] op_sel_hi:[0,1,1]
	v_pk_fma_f32 v[20:21], v[46:47], v[134:135], v[20:21] op_sel_hi:[0,1,1]
	v_pk_fma_f32 v[20:21], v[60:61], v[148:149], v[20:21] op_sel_hi:[0,1,1]
	v_pk_fma_f32 v[20:21], v[64:65], v[164:165], v[20:21] op_sel_hi:[0,1,1]
	v_pk_fma_f32 v[20:21], v[70:71], v[178:179], v[20:21] op_sel_hi:[0,1,1]
	s_waitcnt lgkmcnt(1)
; #define LAS __attribute__((address_space(3)))
; DI const float* inp(kptr_t k, int i) { return (const float*)k[i]; }
; DI void p_adaln_unit(Frame& F, int unit) {
;     ...
;         for (int kk = 0; kk < 32; ++kk) { const int k = F.wave * 128 + k0 + kk; const float w = wv[kk];
;             const LAS f32x4* cp = (const LAS f32x4*)(condT + k * 16);
; #pragma unroll
;             for (int q = 0; q < 4; ++q) { const f32x4 cv = cp[q]; acc[4 * q] += cv[0] * w; acc[4 * q + 1] += cv[1] * w; acc[4 * q + 2] += cv[2] * w; acc[4 * q + 3] += cv[3] * w; } } }
; #pragma unroll
;     for (int b = 0; b < 16; ++b) part[(F.wave * 16 + b) * 64 + F.lane] = acc[b];
;     __syncthreads();
;     float* mod = (float*)(F.ws + WS_MOD);
;     for (int o = F.tid; o < 1024; o += 512) { const int b = o >> 6, col = o & 63; float s = inp(KA, I_BADA)[(size_t)l * NMOD * D + cb * 64 + col];
; #pragma unroll
;         for (int w = 0; w < 8; ++w) s += part[(w * 16 + b) * 64 + col];
;         mod[((size_t)l * NB + b) * (NMOD * D) + cb * 64 + col] = s; }
	v_pk_fma_f32 v[16:17], v[74:75], v[16:17], v[20:21] op_sel_hi:[0,1,1]
	v_pk_fma_f32 v[20:21], v[26:27], v[84:85], v[200:201] op_sel_hi:[0,1,1]
	v_pk_fma_f32 v[20:21], v[30:31], v[38:39], v[20:21] op_sel_hi:[0,1,1]
	v_pk_fma_f32 v[20:21], v[8:9], v[58:59], v[20:21] op_sel_hi:[0,1,1]
	v_pk_fma_f32 v[20:21], v[40:41], v[90:91], v[20:21] op_sel_hi:[0,1,1]
	v_pk_fma_f32 v[20:21], v[24:25], v[106:107], v[20:21] op_sel_hi:[0,1,1]
	v_pk_fma_f32 v[20:21], v[50:51], v[120:121], v[20:21] op_sel_hi:[0,1,1]
	v_pk_fma_f32 v[20:21], v[46:47], v[136:137], v[20:21] op_sel_hi:[0,1,1]
	v_pk_fma_f32 v[20:21], v[60:61], v[150:151], v[20:21] op_sel_hi:[0,1,1]
	v_pk_fma_f32 v[20:21], v[64:65], v[166:167], v[20:21] op_sel_hi:[0,1,1]
	v_pk_fma_f32 v[20:21], v[70:71], v[180:181], v[20:21] op_sel_hi:[0,1,1]
	v_pk_fma_f32 v[20:21], v[74:75], v[18:19], v[20:21] op_sel_hi:[0,1,1]
	v_pk_fma_f32 v[18:19], v[26:27], v[86:87], v[22:23] op_sel_hi:[0,1,1]
	v_pk_fma_f32 v[18:19], v[30:31], v[42:43], v[18:19] op_sel_hi:[0,1,1]
	v_pk_fma_f32 v[18:19], v[8:9], v[62:63], v[18:19] op_sel_hi:[0,1,1]
	v_pk_fma_f32 v[10:11], v[8:9], v[48:49], v[10:11] op_sel_hi:[0,1,1]
	v_pk_fma_f32 v[18:19], v[40:41], v[92:93], v[18:19] op_sel_hi:[0,1,1]
	v_mov_b32_e32 v191, v203
	v_mul_f32_e32 v44, v30, v44
	v_pk_fma_f32 v[10:11], v[40:41], v[66:67], v[10:11] op_sel_hi:[0,1,1]
	v_pk_fma_f32 v[18:19], v[24:25], v[108:109], v[18:19] op_sel_hi:[0,1,1]
	v_pk_add_f32 v[28:29], v[28:29], v[190:191]
	v_mov_b32_e32 v45, v80
	v_pk_fma_f32 v[6:7], v[24:25], v[96:97], v[6:7] op_sel_hi:[0,1,1]
	v_pk_fma_f32 v[10:11], v[24:25], v[98:99], v[10:11] op_sel_hi:[0,1,1]
	v_pk_fma_f32 v[18:19], v[50:51], v[122:123], v[18:19] op_sel_hi:[0,1,1]
	v_pk_add_f32 v[28:29], v[28:29], v[44:45]
	v_mov_b32_e32 v69, v81
	v_mul_f32_e32 v94, v40, v94
	v_pk_fma_f32 v[6:7], v[50:51], v[110:111], v[6:7] op_sel_hi:[0,1,1]
	v_pk_fma_f32 v[10:11], v[50:51], v[112:113], v[10:11] op_sel_hi:[0,1,1]
	v_pk_fma_f32 v[18:19], v[46:47], v[138:139], v[18:19] op_sel_hi:[0,1,1]
	v_pk_add_f32 v[28:29], v[28:29], v[68:69]
	v_mov_b32_e32 v95, v204
	v_pk_fma_f32 v[6:7], v[46:47], v[126:127], v[6:7] op_sel_hi:[0,1,1]
	v_pk_fma_f32 v[10:11], v[46:47], v[128:129], v[10:11] op_sel_hi:[0,1,1]
	v_pk_fma_f32 v[18:19], v[60:61], v[152:153], v[18:19] op_sel_hi:[0,1,1]
	v_pk_add_f32 v[28:29], v[28:29], v[94:95]
	v_mov_b32_e32 v193, v205
	v_mul_f32_e32 v124, v50, v124
	v_pk_fma_f32 v[6:7], v[60:61], v[140:141], v[6:7] op_sel_hi:[0,1,1]
	v_pk_fma_f32 v[10:11], v[60:61], v[142:143], v[10:11] op_sel_hi:[0,1,1]
	v_pk_fma_f32 v[18:19], v[64:65], v[168:169], v[18:19] op_sel_hi:[0,1,1]
	v_pk_add_f32 v[28:29], v[28:29], v[192:193]
	v_mov_b32_e32 v125, v206
	v_pk_fma_f32 v[6:7], v[64:65], v[156:157], v[6:7] op_sel_hi:[0,1,1]
	v_pk_fma_f32 v[10:11], v[64:65], v[158:159], v[10:11] op_sel_hi:[0,1,1]
	v_pk_fma_f32 v[18:19], v[70:71], v[182:183], v[18:19] op_sel_hi:[0,1,1]
	v_pk_add_f32 v[28:29], v[28:29], v[124:125]
	v_mov_b32_e32 v203, v207
	v_mul_f32_e32 v154, v60, v154
	v_pk_fma_f32 v[6:7], v[70:71], v[170:171], v[6:7] op_sel_hi:[0,1,1]
	v_pk_fma_f32 v[10:11], v[70:71], v[172:173], v[10:11] op_sel_hi:[0,1,1]
	s_waitcnt lgkmcnt(0)
	v_pk_fma_f32 v[22:23], v[74:75], v[32:33], v[18:19] op_sel_hi:[0,1,1]
	v_mul_f32_e32 v18, v74, v34
	v_mov_b32_e32 v71, v74
	v_mov_b32_e32 v34, v185
	v_pk_add_f32 v[28:29], v[28:29], v[202:203]
	v_mov_b32_e32 v155, v210
	v_pk_mul_f32 v[26:27], v[70:71], v[34:35]
	v_pk_add_f32 v[28:29], v[28:29], v[154:155]
	v_mov_b32_e32 v209, v211
	v_mul_f32_e32 v184, v70, v184
	v_pk_add_f32 v[28:29], v[28:29], v[208:209]
	v_mov_b32_e32 v185, v26
	v_pk_add_f32 v[28:29], v[28:29], v[184:185]
	v_mov_b32_e32 v19, v27
	v_pk_fma_f32 v[6:7], v[74:75], v[186:187], v[6:7] op_sel_hi:[0,1,1]
	v_pk_fma_f32 v[10:11], v[74:75], v[188:189], v[10:11] op_sel_hi:[0,1,1]
	v_pk_add_f32 v[18:19], v[28:29], v[18:19]
	v_lshl_add_u64 v[4:5], v[4:5], 0, s[10:11]
	s_cbranch_scc0 .LBB0_12
	s_lshl_b32 s10, s97, 12
	s_add_i32 s10, s10, 0
	v_lshl_add_u32 v1, v2, 2, s10
	v_add_u32_e32 v1, 0x10000, v1
	v_cmp_gt_i32_e32 vcc, s96, v0
	ds_write2st64_b32 v1, v6, v7 offset1:1
	ds_write2st64_b32 v1, v10, v11 offset0:2 offset1:3
	ds_write2st64_b32 v1, v12, v13 offset0:4 offset1:5
	ds_write2st64_b32 v1, v14, v15 offset0:6 offset1:7
	ds_write2st64_b32 v1, v16, v17 offset0:8 offset1:9
	ds_write2st64_b32 v1, v20, v21 offset0:10 offset1:11
	ds_write2st64_b32 v1, v22, v23 offset0:12 offset1:13
	ds_write2st64_b32 v1, v18, v19 offset0:14 offset1:15
	s_waitcnt lgkmcnt(0)
	s_barrier
	s_and_saveexec_b64 s[10:11], vcc
	s_cbranch_execz .LBB0_16
	s_load_dwordx2 s[4:5], s[4:5], 0x20
	s_add_u32 s14, s66, s8
	s_addc_u32 s15, s67, s9
	s_and_b64 s[44:45], s[6:7], exec
	s_cselect_b32 s13, 0x6000, 0
	s_waitcnt lgkmcnt(0)
	s_add_u32 s4, s4, s13
	s_addc_u32 s5, s5, 0
	s_add_u32 s4, s4, s8
	s_addc_u32 s5, s5, s9
	v_lshlrev_b32_e32 v1, 2, v2
	s_and_b64 s[6:7], s[6:7], exec
	v_and_b32_e32 v8, 0xfc, v1
	s_cselect_b32 s6, 16, 0
	v_lshl_add_u64 v[2:3], s[4:5], 0, v[8:9]
	s_add_i32 s4, 0, 0x10000
	v_add_u32_e32 v1, s4, v8
	v_lshl_add_u64 v[4:5], s[14:15], 0, v[8:9]
	s_mov_b64 s[4:5], 0

; DI unsigned pk4_fp8(float a, float b, float c, float d) { int r = 0; r = __builtin_amdgcn_cvt_pk_fp8_f32(sat8(a), sat8(b), r, false); r = __builtin_amdgcn_cvt_pk_fp8_f32(sat8(c), sat8(d), r, true); return (unsigned)r; }
; DI void store_pair8(unsigned char* base, size_t off0, size_t off1, const u32x2& w0, const u32x2& w1, bool oddq) {
;     const auto rx = __builtin_amdgcn_permlane16_swap(w0.x, w1.x, false, false), ry = __builtin_amdgcn_permlane16_swap(w0.y, w1.y, false, false);
;     u32x4 ww; ww.x = rx[0]; ww.y = ry[0]; ww.z = rx[1]; ww.w = ry[1];
;     *(u32x4*)(base + (oddq ? off1 - 8 : off0)) = ww;
; }
;     DI void operator()(const f32x4 (&acc)[2][2][4][2], const Unit& u, int wr, int wc, int fr, int fq) const {
;         const float s2 = sc * GATE8_SCALE; const bool oddq = (fq & 1) != 0;
; #pragma unroll
;         for (int ai = 0; ai < 2; ++ai)
; #pragma unroll
;             for (int p2 = 0; p2 < 2; ++p2) { const size_t row0 = (size_t)u.pm * 256 + 128 * ai + 64 * wr + 32 * p2 + fr;
; #pragma unroll
;                 for (int bj = 0; bj < 2; ++bj) { u32x2 w[2];
; #pragma unroll
;                     for (int r2 = 0; r2 < 2; ++r2) { const f32x4 a = acc[ai][bj][2 * p2 + r2][0] * s2, b = acc[ai][bj][2 * p2 + r2][1] * s2; w[r2].x = pk4_fp8(a[0], a[1], a[2], a[3]); w[r2].y = pk4_fp8(b[0], b[1], b[2], b[3]); }
;                     const size_t c = (size_t)(u.pn * 256 + bj * 128 + 32 * wc + 8 * fq);
;                     store_pair8(o, row0 * D + c, (row0 + 16) * D + c, w[0], w[1], oddq); } }
.LBB0_247:
	s_mov_b32 s0, s51
	s_mov_b32 s1, -1
	s_ashr_i32 s23, s0, 2
	v_mbcnt_lo_u32_b32 v0, s1, 0
	v_mbcnt_hi_u32_b32 v0, s1, v0
	s_and_b32 s21, s0, 3
	s_cmp_gt_i32 s33, 3
	v_and_b32_e32 v142, 15, v0
	v_ashrrev_i32_e32 v143, 4, v0
	s_mov_b64 s[2:3], -1
	s_cbranch_scc0 .LBB0_257
	s_add_i32 s28, s33, -4
	s_cmp_gt_u32 s28, 1
	s_cbranch_scc0 .LBB0_254
	s_cmp_gt_u32 s28, 3
	s_cbranch_scc0 .LBB0_251
	s_cmp_lt_u32 s28, 8
	s_mov_b32 s0, 0x2ac00000
	s_cselect_b32 s0, s0, 0x2ec00000
	s_add_u32 s2, s6, s0
	s_addc_u32 s3, s7, 0
	s_ashr_i32 s19, s18, 31
	s_lshl_b64 s[0:1], s[18:19], 8
	s_lshl_b32 s19, s23, 6
	s_ashr_i32 s29, s19, 31
	s_add_u32 s0, s0, s19
	s_addc_u32 s1, s1, s29
	v_or_b32_e32 v132, s0, v142
	s_lshl_b32 s0, s33, 8
	v_mov_b32_e32 v133, s1
	s_and_b32 s0, s0, 0x300
	s_lshl_b32 s1, s21, 5
	s_or_b32 s0, s1, s0
	v_lshl_add_u32 v130, v143, 3, s0
	v_lshlrev_b64 v[132:133], 10, v[132:133]
	s_mov_b64 s[0:1], 0x3ff8
	v_lshl_add_u64 v[144:145], v[132:133], 0, s[0:1]
	s_mov_b32 s0, 0x3c800000
	v_pk_mul_f32 v[134:135], v[126:127], s[0:1] op_sel_hi:[1,0]
	v_pk_mul_f32 v[136:137], v[128:129], s[0:1] op_sel_hi:[1,0]
	v_pk_mul_f32 v[148:149], v[122:123], s[0:1] op_sel_hi:[1,0]
	v_med3_f32 v131, v134, s53, v204
	v_med3_f32 v135, v135, s53, v204
	v_mov_b32_e32 v134, v1
	v_cvt_pk_fp8_f32 v134, v131, v135
	v_med3_f32 v131, v136, s53, v204
	v_med3_f32 v136, v137, s53, v204
	v_med3_f32 v137, v148, s53, v204
	v_med3_f32 v148, v149, s53, v204
	v_mov_b32_e32 v135, v1
	v_cvt_pk_fp8_f32 v135, v137, v148
	v_pk_mul_f32 v[146:147], v[124:125], s[0:1] op_sel_hi:[1,0]
	v_cvt_pk_fp8_f32 v134, v131, v136 op_sel:[0,0,1]
	v_med3_f32 v131, v146, s53, v204
	v_med3_f32 v136, v147, s53, v204
	v_cvt_pk_fp8_f32 v135, v131, v136 op_sel:[0,0,1]
	v_pk_mul_f32 v[136:137], v[118:119], s[0:1] op_sel_hi:[1,0]
	v_pk_mul_f32 v[146:147], v[120:121], s[0:1] op_sel_hi:[1,0]
	v_pk_mul_f32 v[150:151], v[110:111], s[0:1] op_sel_hi:[1,0]
	v_med3_f32 v131, v136, s53, v204
	v_med3_f32 v137, v137, s53, v204
	v_mov_b32_e32 v136, v1
	v_cvt_pk_fp8_f32 v136, v131, v137
	v_med3_f32 v131, v146, s53, v204
	v_med3_f32 v146, v147, s53, v204
	v_med3_f32 v147, v150, s53, v204
	v_med3_f32 v150, v151, s53, v204
	v_mov_b32_e32 v137, v1
	v_cvt_pk_fp8_f32 v137, v147, v150
	v_pk_mul_f32 v[148:149], v[112:113], s[0:1] op_sel_hi:[1,0]
	v_cvt_pk_fp8_f32 v136, v131, v146 op_sel:[0,0,1]
	v_med3_f32 v131, v148, s53, v204
	v_med3_f32 v146, v149, s53, v204
	v_and_b32_e32 v0, 16, v0
	v_cvt_pk_fp8_f32 v137, v131, v146 op_sel:[0,0,1]
	v_cmp_eq_u32_e32 vcc, 0, v0
	v_ashrrev_i32_e32 v131, 31, v130
	v_permlane16_swap_b32_e32 v134, v136
	v_cndmask_b32_e32 v145, v145, v133, vcc
	v_cndmask_b32_e32 v144, v144, v132, vcc
	v_lshl_add_u64 v[144:145], s[2:3], 0, v[144:145]
	v_permlane16_swap_b32_e32 v135, v137
	v_lshl_add_u64 v[144:145], v[144:145], 0, v[130:131]
	global_store_dwordx4 v[144:145], v[134:137], off nt
	v_pk_mul_f32 v[148:149], v[106:107], s[0:1] op_sel_hi:[1,0]
	v_pk_mul_f32 v[146:147], v[108:109], s[0:1] op_sel_hi:[1,0]
	v_pk_mul_f32 v[134:135], v[114:115], s[0:1] op_sel_hi:[1,0]
	v_pk_mul_f32 v[136:137], v[116:117], s[0:1] op_sel_hi:[1,0]
	v_med3_f32 v0, v134, s53, v204
	v_med3_f32 v135, v135, s53, v204
	v_mov_b32_e32 v134, v1
	v_cvt_pk_fp8_f32 v134, v0, v135
	v_med3_f32 v0, v136, s53, v204
	v_med3_f32 v136, v137, s53, v204
	v_med3_f32 v137, v148, s53, v204
	v_med3_f32 v148, v149, s53, v204
	v_mov_b32_e32 v135, v1
	v_cvt_pk_fp8_f32 v135, v137, v148
	v_cvt_pk_fp8_f32 v134, v0, v136 op_sel:[0,0,1]
	v_med3_f32 v0, v146, s53, v204
	v_med3_f32 v136, v147, s53, v204
	v_cvt_pk_fp8_f32 v135, v0, v136 op_sel:[0,0,1]
	v_pk_mul_f32 v[136:137], v[98:99], s[0:1] op_sel_hi:[1,0]
	v_pk_mul_f32 v[146:147], v[100:101], s[0:1] op_sel_hi:[1,0]
	v_pk_mul_f32 v[150:151], v[90:91], s[0:1] op_sel_hi:[1,0]
	v_med3_f32 v0, v136, s53, v204
	v_med3_f32 v137, v137, s53, v204
	v_mov_b32_e32 v136, v1
	v_cvt_pk_fp8_f32 v136, v0, v137
	v_med3_f32 v0, v146, s53, v204
	v_med3_f32 v146, v147, s53, v204
	v_med3_f32 v147, v150, s53, v204
	v_med3_f32 v150, v151, s53, v204
	v_mov_b32_e32 v137, v1
	v_cvt_pk_fp8_f32 v137, v147, v150
	v_pk_mul_f32 v[148:149], v[92:93], s[0:1] op_sel_hi:[1,0]
	v_cvt_pk_fp8_f32 v136, v0, v146 op_sel:[0,0,1]
	v_med3_f32 v0, v148, s53, v204
	v_med3_f32 v146, v149, s53, v204
	v_cvt_pk_fp8_f32 v137, v0, v146 op_sel:[0,0,1]
	v_permlane16_swap_b32_e32 v134, v136
	v_pk_mul_f32 v[148:149], v[94:95], s[0:1] op_sel_hi:[1,0]
	v_permlane16_swap_b32_e32 v135, v137
	global_store_dwordx4 v[144:145], v[134:137], off offset:128 nt
	v_med3_f32 v148, v148, s53, v204
	v_med3_f32 v149, v149, s53, v204
	v_pk_mul_f32 v[134:135], v[102:103], s[0:1] op_sel_hi:[1,0]
	v_pk_mul_f32 v[136:137], v[104:105], s[0:1] op_sel_hi:[1,0]
	v_med3_f32 v150, v134, s53, v204
	v_med3_f32 v135, v135, s53, v204
	v_mov_b32_e32 v134, v1
	v_cvt_pk_fp8_f32 v134, v150, v135
	v_mov_b32_e32 v135, v1
	v_cvt_pk_fp8_f32 v135, v148, v149
	v_pk_mul_f32 v[146:147], v[96:97], s[0:1] op_sel_hi:[1,0]
	v_med3_f32 v136, v136, s53, v204
	v_med3_f32 v137, v137, s53, v204
	v_cvt_pk_fp8_f32 v134, v136, v137 op_sel:[0,0,1]
	v_med3_f32 v136, v146, s53, v204
	v_med3_f32 v137, v147, s53, v204
	v_cvt_pk_fp8_f32 v135, v136, v137 op_sel:[0,0,1]
	v_pk_mul_f32 v[136:137], v[86:87], s[0:1] op_sel_hi:[1,0]
	v_pk_mul_f32 v[150:151], v[78:79], s[0:1] op_sel_hi:[1,0]
	v_med3_f32 v152, v136, s53, v204
	v_med3_f32 v137, v137, s53, v204
	v_mov_b32_e32 v136, v1
	v_cvt_pk_fp8_f32 v136, v152, v137
	v_med3_f32 v150, v150, s53, v204
	v_med3_f32 v151, v151, s53, v204
	v_mov_b32_e32 v137, v1
	v_cvt_pk_fp8_f32 v137, v150, v151
	v_pk_mul_f32 v[146:147], v[88:89], s[0:1] op_sel_hi:[1,0]
; DI unsigned pk4_fp8(float a, float b, float c, float d) { int r = 0; r = __builtin_amdgcn_cvt_pk_fp8_f32(sat8(a), sat8(b), r, false); r = __builtin_amdgcn_cvt_pk_fp8_f32(sat8(c), sat8(d), r, true); return (unsigned)r; }
; DI void store_pair8(unsigned char* base, size_t off0, size_t off1, const u32x2& w0, const u32x2& w1, bool oddq) {
;     const auto rx = __builtin_amdgcn_permlane16_swap(w0.x, w1.x, false, false), ry = __builtin_amdgcn_permlane16_swap(w0.y, w1.y, false, false);
;     u32x4 ww; ww.x = rx[0]; ww.y = ry[0]; ww.z = rx[1]; ww.w = ry[1];
;     *(u32x4*)(base + (oddq ? off1 - 8 : off0)) = ww;
; }
;     DI void operator()(const f32x4 (&acc)[2][2][4][2], const Unit& u, int wr, int wc, int fr, int fq) const {
;         const float s2 = sc * GATE8_SCALE; const bool oddq = (fq & 1) != 0;
; #pragma unroll
;         for (int ai = 0; ai < 2; ++ai)
; #pragma unroll
;             for (int p2 = 0; p2 < 2; ++p2) { const size_t row0 = (size_t)u.pm * 256 + 128 * ai + 64 * wr + 32 * p2 + fr;
; #pragma unroll
;                 for (int bj = 0; bj < 2; ++bj) { u32x2 w[2];
; #pragma unroll
;                     for (int r2 = 0; r2 < 2; ++r2) { const f32x4 a = acc[ai][bj][2 * p2 + r2][0] * s2, b = acc[ai][bj][2 * p2 + r2][1] * s2; w[r2].x = pk4_fp8(a[0], a[1], a[2], a[3]); w[r2].y = pk4_fp8(b[0], b[1], b[2], b[3]); }
;                     const size_t c = (size_t)(u.pn * 256 + bj * 128 + 32 * wc + 8 * fq);
;                     store_pair8(o, row0 * D + c, (row0 + 16) * D + c, w[0], w[1], oddq); } }
	v_pk_mul_f32 v[148:149], v[80:81], s[0:1] op_sel_hi:[1,0]
	v_med3_f32 v146, v146, s53, v204
	v_med3_f32 v147, v147, s53, v204
	v_cvt_pk_fp8_f32 v136, v146, v147 op_sel:[0,0,1]
	v_med3_f32 v146, v148, s53, v204
	v_med3_f32 v147, v149, s53, v204
	s_mov_b64 s[30:31], 0xbff8
	v_cvt_pk_fp8_f32 v137, v146, v147 op_sel:[0,0,1]
	v_or_b32_e32 v0, 0x8000, v132
	v_lshl_add_u64 v[144:145], v[132:133], 0, s[30:31]
	v_cndmask_b32_e32 v145, v145, v133, vcc
	v_cndmask_b32_e32 v144, v144, v0, vcc
	v_lshl_add_u64 v[144:145], s[2:3], 0, v[144:145]
	v_permlane16_swap_b32_e32 v134, v136
	v_permlane16_swap_b32_e32 v135, v137
	v_lshl_add_u64 v[144:145], v[144:145], 0, v[130:131]
	global_store_dwordx4 v[144:145], v[134:137], off nt
	v_pk_mul_f32 v[148:149], v[74:75], s[0:1] op_sel_hi:[1,0]
	v_pk_mul_f32 v[146:147], v[76:77], s[0:1] op_sel_hi:[1,0]
	v_pk_mul_f32 v[134:135], v[82:83], s[0:1] op_sel_hi:[1,0]
	v_pk_mul_f32 v[136:137], v[84:85], s[0:1] op_sel_hi:[1,0]
	v_med3_f32 v0, v134, s53, v204
	v_med3_f32 v135, v135, s53, v204
	v_mov_b32_e32 v134, v1
	v_cvt_pk_fp8_f32 v134, v0, v135
	v_med3_f32 v0, v136, s53, v204
	v_med3_f32 v136, v137, s53, v204
	v_med3_f32 v137, v148, s53, v204
	v_med3_f32 v148, v149, s53, v204
	v_mov_b32_e32 v135, v1
	v_cvt_pk_fp8_f32 v135, v137, v148
	v_cvt_pk_fp8_f32 v134, v0, v136 op_sel:[0,0,1]
	v_med3_f32 v0, v146, s53, v204
	v_med3_f32 v136, v147, s53, v204
	v_cvt_pk_fp8_f32 v135, v0, v136 op_sel:[0,0,1]
	v_pk_mul_f32 v[136:137], v[70:71], s[0:1] op_sel_hi:[1,0]
	v_pk_mul_f32 v[146:147], v[72:73], s[0:1] op_sel_hi:[1,0]
	v_pk_mul_f32 v[150:151], v[66:67], s[0:1] op_sel_hi:[1,0]
	v_med3_f32 v0, v136, s53, v204
	v_med3_f32 v137, v137, s53, v204
	v_mov_b32_e32 v136, v1
	v_cvt_pk_fp8_f32 v136, v0, v137
	v_med3_f32 v0, v146, s53, v204
	v_med3_f32 v146, v147, s53, v204
	v_med3_f32 v147, v150, s53, v204
	v_med3_f32 v150, v151, s53, v204
	v_mov_b32_e32 v137, v1
	v_cvt_pk_fp8_f32 v137, v147, v150
	v_pk_mul_f32 v[148:149], v[68:69], s[0:1] op_sel_hi:[1,0]
	v_cvt_pk_fp8_f32 v136, v0, v146 op_sel:[0,0,1]
	v_med3_f32 v0, v148, s53, v204
	v_med3_f32 v146, v149, s53, v204
	v_cvt_pk_fp8_f32 v137, v0, v146 op_sel:[0,0,1]
	v_permlane16_swap_b32_e32 v134, v136
	v_pk_mul_f32 v[146:147], v[58:59], s[0:1] op_sel_hi:[1,0]
	v_permlane16_swap_b32_e32 v135, v137
	global_store_dwordx4 v[144:145], v[134:137], off offset:128 nt
	v_pk_mul_f32 v[144:145], v[60:61], s[0:1] op_sel_hi:[1,0]
	v_pk_mul_f32 v[148:149], v[46:47], s[0:1] op_sel_hi:[1,0]
	v_pk_mul_f32 v[134:135], v[62:63], s[0:1] op_sel_hi:[1,0]
	v_pk_mul_f32 v[136:137], v[64:65], s[0:1] op_sel_hi:[1,0]
	v_med3_f32 v0, v134, s53, v204
	v_med3_f32 v135, v135, s53, v204
	v_mov_b32_e32 v134, v1
	v_cvt_pk_fp8_f32 v134, v0, v135
	v_med3_f32 v0, v136, s53, v204
	v_med3_f32 v136, v137, s53, v204
	v_med3_f32 v137, v146, s53, v204
	v_med3_f32 v146, v147, s53, v204
	v_mov_b32_e32 v135, v1
	v_cvt_pk_fp8_f32 v135, v137, v146
	v_cvt_pk_fp8_f32 v134, v0, v136 op_sel:[0,0,1]
	v_med3_f32 v0, v144, s53, v204
	v_med3_f32 v136, v145, s53, v204
	v_cvt_pk_fp8_f32 v135, v0, v136 op_sel:[0,0,1]
	v_pk_mul_f32 v[136:137], v[54:55], s[0:1] op_sel_hi:[1,0]
	v_pk_mul_f32 v[144:145], v[56:57], s[0:1] op_sel_hi:[1,0]
	v_med3_f32 v0, v136, s53, v204
	v_med3_f32 v137, v137, s53, v204
	v_mov_b32_e32 v136, v1
	v_cvt_pk_fp8_f32 v136, v0, v137
	v_med3_f32 v0, v144, s53, v204
	v_med3_f32 v144, v145, s53, v204
	v_med3_f32 v145, v148, s53, v204
	v_med3_f32 v148, v149, s53, v204
	v_mov_b32_e32 v137, v1
	v_cvt_pk_fp8_f32 v137, v145, v148
	v_pk_mul_f32 v[146:147], v[48:49], s[0:1] op_sel_hi:[1,0]
	v_cvt_pk_fp8_f32 v136, v0, v144 op_sel:[0,0,1]
	v_med3_f32 v0, v146, s53, v204
	v_med3_f32 v144, v147, s53, v204
	v_cvt_pk_fp8_f32 v137, v0, v144 op_sel:[0,0,1]
	v_mov_b32_e32 v0, 0x23ff8
	v_mov_b32_e32 v144, 0x20000
	v_cndmask_b32_e32 v0, v0, v144, vcc
	v_lshl_add_u64 v[144:145], s[2:3], 0, v[132:133]
	v_lshl_add_u64 v[132:133], v[144:145], 0, v[0:1]
	v_permlane16_swap_b32_e32 v134, v136
	v_permlane16_swap_b32_e32 v135, v137
	v_lshl_add_u64 v[146:147], v[132:133], 0, v[130:131]
	v_pk_mul_f32 v[132:133], v[50:51], s[0:1] op_sel_hi:[1,0]
	global_store_dwordx4 v[146:147], v[134:137], off nt
	v_pk_mul_f32 v[148:149], v[42:43], s[0:1] op_sel_hi:[1,0]
	v_med3_f32 v0, v132, s53, v204
	v_pk_mul_f32 v[134:135], v[52:53], s[0:1] op_sel_hi:[1,0]
	v_med3_f32 v133, v133, s53, v204
	v_mov_b32_e32 v132, v1
	v_cvt_pk_fp8_f32 v132, v0, v133
	v_med3_f32 v0, v134, s53, v204
	v_med3_f32 v134, v135, s53, v204
	v_med3_f32 v135, v148, s53, v204
; DI unsigned pk4_fp8(float a, float b, float c, float d) { int r = 0; r = __builtin_amdgcn_cvt_pk_fp8_f32(sat8(a), sat8(b), r, false); r = __builtin_amdgcn_cvt_pk_fp8_f32(sat8(c), sat8(d), r, true); return (unsigned)r; }
; DI void store_pair8(unsigned char* base, size_t off0, size_t off1, const u32x2& w0, const u32x2& w1, bool oddq) {
;     const auto rx = __builtin_amdgcn_permlane16_swap(w0.x, w1.x, false, false), ry = __builtin_amdgcn_permlane16_swap(w0.y, w1.y, false, false);
;     u32x4 ww; ww.x = rx[0]; ww.y = ry[0]; ww.z = rx[1]; ww.w = ry[1];
;     *(u32x4*)(base + (oddq ? off1 - 8 : off0)) = ww;
; }
;     DI void operator()(const f32x4 (&acc)[2][2][4][2], const Unit& u, int wr, int wc, int fr, int fq) const {
;         const float s2 = sc * GATE8_SCALE; const bool oddq = (fq & 1) != 0;
; #pragma unroll
;         for (int ai = 0; ai < 2; ++ai)
; #pragma unroll
;             for (int p2 = 0; p2 < 2; ++p2) { const size_t row0 = (size_t)u.pm * 256 + 128 * ai + 64 * wr + 32 * p2 + fr;
; #pragma unroll
;                 for (int bj = 0; bj < 2; ++bj) { u32x2 w[2];
; #pragma unroll
;                     for (int r2 = 0; r2 < 2; ++r2) { const f32x4 a = acc[ai][bj][2 * p2 + r2][0] * s2, b = acc[ai][bj][2 * p2 + r2][1] * s2; w[r2].x = pk4_fp8(a[0], a[1], a[2], a[3]); w[r2].y = pk4_fp8(b[0], b[1], b[2], b[3]); }
;                     const size_t c = (size_t)(u.pn * 256 + bj * 128 + 32 * wc + 8 * fq);
;                     store_pair8(o, row0 * D + c, (row0 + 16) * D + c, w[0], w[1], oddq); } }
	v_med3_f32 v148, v149, s53, v204
	v_mov_b32_e32 v133, v1
	v_cvt_pk_fp8_f32 v133, v135, v148
	v_pk_mul_f32 v[136:137], v[44:45], s[0:1] op_sel_hi:[1,0]
	v_cvt_pk_fp8_f32 v132, v0, v134 op_sel:[0,0,1]
	v_med3_f32 v0, v136, s53, v204
	v_med3_f32 v134, v137, s53, v204
	v_cvt_pk_fp8_f32 v133, v0, v134 op_sel:[0,0,1]
	v_pk_mul_f32 v[134:135], v[34:35], s[0:1] op_sel_hi:[1,0]
	v_pk_mul_f32 v[136:137], v[36:37], s[0:1] op_sel_hi:[1,0]
	v_pk_mul_f32 v[150:151], v[26:27], s[0:1] op_sel_hi:[1,0]
	v_med3_f32 v0, v134, s53, v204
	v_med3_f32 v135, v135, s53, v204
	v_mov_b32_e32 v134, v1
	v_cvt_pk_fp8_f32 v134, v0, v135
	v_med3_f32 v0, v136, s53, v204
	v_med3_f32 v136, v137, s53, v204
	v_med3_f32 v137, v150, s53, v204
	v_med3_f32 v150, v151, s53, v204
	v_mov_b32_e32 v135, v1
	v_cvt_pk_fp8_f32 v135, v137, v150
	v_pk_mul_f32 v[148:149], v[28:29], s[0:1] op_sel_hi:[1,0]
	v_cvt_pk_fp8_f32 v134, v0, v136 op_sel:[0,0,1]
	v_med3_f32 v0, v148, s53, v204
	v_med3_f32 v136, v149, s53, v204
	v_cvt_pk_fp8_f32 v135, v0, v136 op_sel:[0,0,1]
	v_permlane16_swap_b32_e32 v132, v134
	v_pk_mul_f32 v[136:137], v[32:33], s[0:1] op_sel_hi:[1,0]
	v_permlane16_swap_b32_e32 v133, v135
	global_store_dwordx4 v[146:147], v[132:135], off offset:128 nt
	v_pk_mul_f32 v[146:147], v[30:31], s[0:1] op_sel_hi:[1,0]
	v_pk_mul_f32 v[148:149], v[14:15], s[0:1] op_sel_hi:[1,0]
	v_pk_mul_f32 v[132:133], v[38:39], s[0:1] op_sel_hi:[1,0]
	v_pk_mul_f32 v[134:135], v[40:41], s[0:1] op_sel_hi:[1,0]
	v_med3_f32 v0, v132, s53, v204
	v_med3_f32 v133, v133, s53, v204
	v_mov_b32_e32 v132, v1
	v_cvt_pk_fp8_f32 v132, v0, v133
	v_med3_f32 v0, v134, s53, v204
	v_med3_f32 v134, v135, s53, v204
	v_med3_f32 v135, v146, s53, v204
	v_med3_f32 v146, v147, s53, v204
	v_mov_b32_e32 v133, v1
	v_cvt_pk_fp8_f32 v133, v135, v146
	v_cvt_pk_fp8_f32 v132, v0, v134 op_sel:[0,0,1]
	v_med3_f32 v0, v136, s53, v204
	v_med3_f32 v134, v137, s53, v204
	v_cvt_pk_fp8_f32 v133, v0, v134 op_sel:[0,0,1]
	v_pk_mul_f32 v[134:135], v[22:23], s[0:1] op_sel_hi:[1,0]
	v_pk_mul_f32 v[136:137], v[24:25], s[0:1] op_sel_hi:[1,0]
	v_med3_f32 v0, v134, s53, v204
	v_med3_f32 v135, v135, s53, v204
	v_mov_b32_e32 v134, v1
	v_cvt_pk_fp8_f32 v134, v0, v135
	v_med3_f32 v0, v136, s53, v204
	v_med3_f32 v136, v137, s53, v204
	v_med3_f32 v137, v148, s53, v204
	v_med3_f32 v148, v149, s53, v204
	v_mov_b32_e32 v135, v1
	v_cvt_pk_fp8_f32 v135, v137, v148
	v_pk_mul_f32 v[146:147], v[16:17], s[0:1] op_sel_hi:[1,0]
	v_cvt_pk_fp8_f32 v134, v0, v136 op_sel:[0,0,1]
	v_med3_f32 v0, v146, s53, v204
	v_med3_f32 v136, v147, s53, v204
	v_cvt_pk_fp8_f32 v135, v0, v136 op_sel:[0,0,1]
	v_mov_b32_e32 v0, 0x2bff8
	v_mov_b32_e32 v136, 0x28000
	v_cndmask_b32_e32 v0, v0, v136, vcc
	v_lshl_add_u64 v[136:137], v[144:145], 0, v[0:1]
	v_permlane16_swap_b32_e32 v132, v134
	v_permlane16_swap_b32_e32 v133, v135
	v_lshl_add_u64 v[136:137], v[136:137], 0, v[130:131]
	v_pk_mul_f32 v[130:131], v[18:19], s[0:1] op_sel_hi:[1,0]
	global_store_dwordx4 v[136:137], v[132:135], off nt
	v_pk_mul_f32 v[144:145], v[10:11], s[0:1] op_sel_hi:[1,0]
	v_med3_f32 v0, v130, s53, v204
	v_pk_mul_f32 v[132:133], v[20:21], s[0:1] op_sel_hi:[1,0]
	v_med3_f32 v131, v131, s53, v204
	v_mov_b32_e32 v130, v1
	v_cvt_pk_fp8_f32 v130, v0, v131
	v_med3_f32 v0, v132, s53, v204
	v_med3_f32 v132, v133, s53, v204
	v_med3_f32 v133, v144, s53, v204
	v_med3_f32 v144, v145, s53, v204
	v_mov_b32_e32 v131, v1
	v_cvt_pk_fp8_f32 v131, v133, v144
	v_pk_mul_f32 v[134:135], v[12:13], s[0:1] op_sel_hi:[1,0]
	v_cvt_pk_fp8_f32 v130, v0, v132 op_sel:[0,0,1]
	v_med3_f32 v0, v134, s53, v204
	v_med3_f32 v132, v135, s53, v204
	v_cvt_pk_fp8_f32 v131, v0, v132 op_sel:[0,0,1]
	v_pk_mul_f32 v[132:133], v[6:7], s[0:1] op_sel_hi:[1,0]
	v_pk_mul_f32 v[134:135], v[8:9], s[0:1] op_sel_hi:[1,0]
	v_pk_mul_f32 v[146:147], v[2:3], s[0:1] op_sel_hi:[1,0]
	v_med3_f32 v0, v132, s53, v204
	v_med3_f32 v133, v133, s53, v204
	v_mov_b32_e32 v132, v1
	v_cvt_pk_fp8_f32 v132, v0, v133
	v_med3_f32 v0, v134, s53, v204
	v_med3_f32 v134, v135, s53, v204
	v_med3_f32 v135, v146, s53, v204
	v_med3_f32 v146, v147, s53, v204
	v_mov_b32_e32 v133, v1
	v_cvt_pk_fp8_f32 v133, v135, v146
	v_pk_mul_f32 v[144:145], v[4:5], s[0:1] op_sel_hi:[1,0]
	v_cvt_pk_fp8_f32 v132, v0, v134 op_sel:[0,0,1]
	v_med3_f32 v0, v144, s53, v204
	v_med3_f32 v134, v145, s53, v204
	v_cvt_pk_fp8_f32 v133, v0, v134 op_sel:[0,0,1]
	v_permlane16_swap_b32_e32 v130, v132
	s_mov_b64 s[2:3], 0
	v_permlane16_swap_b32_e32 v131, v133
	global_store_dwordx4 v[136:137], v[130:133], off offset:128 nt

; DI void phase_scan(Frame& F, int l) {
;     ...
;     for (int u = F.bid; u < NG * 2; u += F.G) { const int g = u >> 1, b = (u & 1) * 8 + (F.tid >> 6), p = F.tid & 63;
;         const float lr = l32[(g * SP + p) * 2], li = l32[(g * SP + p) * 2 + 1];
;         const size_t row0 = (size_t)g * CROWS + b * NCH; float sr = 0.f, si = 0.f;
;         f32x2 ev[NCH];
; #pragma unroll
;         for (int k = 0; k < NCH; ++k) ev[k] = *(const f32x2*)(E + (row0 + k) * 128 + 2 * p);
.LBB0_397:
	s_ashr_i32 s0, s2, 1
	s_and_b32 s6, s3, 0x200
	v_lshl_or_b32 v6, s0, 7, v2
	v_ashrrev_i32_e32 v7, 31, v6
	v_add_u32_e32 v0, s6, v3
	v_lshl_add_u64 v[132:133], v[6:7], 2, s[4:5]
	s_ashr_i32 s1, s0, 31
	v_and_b32_e32 v6, 0xffffffc0, v0
	s_lshl_b64 s[0:1], s[0:1], 10
	v_ashrrev_i32_e32 v7, 31, v6
	v_lshl_add_u64 v[134:135], s[0:1], 0, v[6:7]
	v_lshlrev_b64 v[6:7], 9, v[134:135]
	v_lshl_add_u64 v[8:9], v[4:5], 0, v[6:7]
	global_load_dwordx2 v[130:131], v[8:9], off nt
	v_mov_b64_e32 v[136:137], s[10:11]
	global_load_dwordx2 v[132:133], v[132:133], off nt
	v_or_b32_e32 v8, 0x200, v6
	v_mov_b32_e32 v9, v7
	v_lshl_add_u64 v[8:9], v[4:5], 0, v[8:9]
	global_load_dwordx2 v[128:129], v[8:9], off nt
	v_or_b32_e32 v8, 0x400, v6
	v_mov_b32_e32 v9, v7
	v_lshl_add_u64 v[8:9], v[4:5], 0, v[8:9]
	global_load_dwordx2 v[126:127], v[8:9], off nt
	v_or_b32_e32 v8, 0x600, v6
	v_mov_b32_e32 v9, v7
	v_lshl_add_u64 v[8:9], v[4:5], 0, v[8:9]
	global_load_dwordx2 v[124:125], v[8:9], off nt
	v_or_b32_e32 v8, 0x800, v6
	v_mov_b32_e32 v9, v7
	v_lshl_add_u64 v[8:9], v[4:5], 0, v[8:9]
	global_load_dwordx2 v[122:123], v[8:9], off nt
	v_or_b32_e32 v8, 0xa00, v6
	v_mov_b32_e32 v9, v7
	v_lshl_add_u64 v[8:9], v[4:5], 0, v[8:9]
	global_load_dwordx2 v[120:121], v[8:9], off nt
	v_or_b32_e32 v8, 0xc00, v6
	v_mov_b32_e32 v9, v7
	v_lshl_add_u64 v[8:9], v[4:5], 0, v[8:9]
	global_load_dwordx2 v[118:119], v[8:9], off nt
	v_or_b32_e32 v8, 0xe00, v6
	v_mov_b32_e32 v9, v7
	v_lshl_add_u64 v[8:9], v[4:5], 0, v[8:9]
	global_load_dwordx2 v[116:117], v[8:9], off nt
	v_or_b32_e32 v8, 0x1000, v6
	v_mov_b32_e32 v9, v7
	v_lshl_add_u64 v[8:9], v[4:5], 0, v[8:9]
	global_load_dwordx2 v[114:115], v[8:9], off nt
	v_or_b32_e32 v8, 0x1200, v6
	v_mov_b32_e32 v9, v7
	v_lshl_add_u64 v[8:9], v[4:5], 0, v[8:9]
	global_load_dwordx2 v[112:113], v[8:9], off nt
	v_or_b32_e32 v8, 0x1400, v6
	v_mov_b32_e32 v9, v7
	v_lshl_add_u64 v[8:9], v[4:5], 0, v[8:9]
	global_load_dwordx2 v[110:111], v[8:9], off nt
	v_or_b32_e32 v8, 0x1600, v6
	v_mov_b32_e32 v9, v7
	v_lshl_add_u64 v[8:9], v[4:5], 0, v[8:9]
	global_load_dwordx2 v[108:109], v[8:9], off nt
	v_or_b32_e32 v8, 0x1800, v6
	v_mov_b32_e32 v9, v7
	v_lshl_add_u64 v[8:9], v[4:5], 0, v[8:9]
	global_load_dwordx2 v[106:107], v[8:9], off nt
	v_or_b32_e32 v8, 0x1a00, v6
	v_mov_b32_e32 v9, v7
	v_lshl_add_u64 v[8:9], v[4:5], 0, v[8:9]
	global_load_dwordx2 v[104:105], v[8:9], off nt
	v_or_b32_e32 v8, 0x1c00, v6
	v_mov_b32_e32 v9, v7
	v_lshl_add_u64 v[8:9], v[4:5], 0, v[8:9]
	global_load_dwordx2 v[102:103], v[8:9], off nt
	v_or_b32_e32 v8, 0x1e00, v6
	v_mov_b32_e32 v9, v7
	v_lshl_add_u64 v[8:9], v[4:5], 0, v[8:9]
	global_load_dwordx2 v[100:101], v[8:9], off nt
	v_or_b32_e32 v8, 0x2000, v6
	v_mov_b32_e32 v9, v7
	v_lshl_add_u64 v[8:9], v[4:5], 0, v[8:9]
	global_load_dwordx2 v[98:99], v[8:9], off nt
	v_or_b32_e32 v8, 0x2200, v6
	v_mov_b32_e32 v9, v7
	v_lshl_add_u64 v[8:9], v[4:5], 0, v[8:9]
	global_load_dwordx2 v[96:97], v[8:9], off nt
	v_or_b32_e32 v8, 0x2400, v6
	v_mov_b32_e32 v9, v7
	v_lshl_add_u64 v[8:9], v[4:5], 0, v[8:9]
	global_load_dwordx2 v[94:95], v[8:9], off nt
	v_or_b32_e32 v8, 0x2600, v6
	v_mov_b32_e32 v9, v7
	v_lshl_add_u64 v[8:9], v[4:5], 0, v[8:9]
	global_load_dwordx2 v[92:93], v[8:9], off nt
	v_or_b32_e32 v8, 0x2800, v6
	v_mov_b32_e32 v9, v7
	v_lshl_add_u64 v[8:9], v[4:5], 0, v[8:9]
	global_load_dwordx2 v[90:91], v[8:9], off nt
	v_or_b32_e32 v8, 0x2a00, v6
	v_mov_b32_e32 v9, v7
	v_lshl_add_u64 v[8:9], v[4:5], 0, v[8:9]
	global_load_dwordx2 v[88:89], v[8:9], off nt
	v_or_b32_e32 v8, 0x2c00, v6
	v_mov_b32_e32 v9, v7
	v_lshl_add_u64 v[8:9], v[4:5], 0, v[8:9]
	global_load_dwordx2 v[86:87], v[8:9], off nt
	v_or_b32_e32 v8, 0x2e00, v6
	v_mov_b32_e32 v9, v7
	v_lshl_add_u64 v[8:9], v[4:5], 0, v[8:9]
	global_load_dwordx2 v[84:85], v[8:9], off nt
	v_or_b32_e32 v8, 0x3000, v6
	v_mov_b32_e32 v9, v7
	v_lshl_add_u64 v[8:9], v[4:5], 0, v[8:9]
	global_load_dwordx2 v[82:83], v[8:9], off nt
	v_or_b32_e32 v8, 0x3200, v6
	v_mov_b32_e32 v9, v7
	v_lshl_add_u64 v[8:9], v[4:5], 0, v[8:9]
	global_load_dwordx2 v[80:81], v[8:9], off nt
	v_or_b32_e32 v8, 0x3400, v6
	v_mov_b32_e32 v9, v7
	v_lshl_add_u64 v[8:9], v[4:5], 0, v[8:9]
	global_load_dwordx2 v[78:79], v[8:9], off nt
	v_or_b32_e32 v8, 0x3600, v6
	v_mov_b32_e32 v9, v7
	v_lshl_add_u64 v[8:9], v[4:5], 0, v[8:9]
	global_load_dwordx2 v[76:77], v[8:9], off nt
	v_or_b32_e32 v8, 0x3800, v6
	v_mov_b32_e32 v9, v7
	v_lshl_add_u64 v[8:9], v[4:5], 0, v[8:9]
	global_load_dwordx2 v[74:75], v[8:9], off nt
	v_or_b32_e32 v8, 0x3a00, v6
	v_mov_b32_e32 v9, v7
	v_lshl_add_u64 v[8:9], v[4:5], 0, v[8:9]
	global_load_dwordx2 v[72:73], v[8:9], off nt
	v_or_b32_e32 v8, 0x3c00, v6
	v_mov_b32_e32 v9, v7
	v_lshl_add_u64 v[8:9], v[4:5], 0, v[8:9]
	global_load_dwordx2 v[70:71], v[8:9], off nt
	v_or_b32_e32 v8, 0x3e00, v6
	v_mov_b32_e32 v9, v7
	v_lshl_add_u64 v[8:9], v[4:5], 0, v[8:9]
	global_load_dwordx2 v[68:69], v[8:9], off nt
	v_or_b32_e32 v8, 0x4000, v6
	v_mov_b32_e32 v9, v7
	v_lshl_add_u64 v[8:9], v[4:5], 0, v[8:9]
	global_load_dwordx2 v[66:67], v[8:9], off nt
	v_or_b32_e32 v8, 0x4200, v6
	v_mov_b32_e32 v9, v7
	v_lshl_add_u64 v[8:9], v[4:5], 0, v[8:9]
	global_load_dwordx2 v[64:65], v[8:9], off nt
	v_or_b32_e32 v8, 0x4400, v6
	v_mov_b32_e32 v9, v7
	v_lshl_add_u64 v[8:9], v[4:5], 0, v[8:9]
	global_load_dwordx2 v[62:63], v[8:9], off nt
	v_or_b32_e32 v8, 0x4600, v6
	v_mov_b32_e32 v9, v7
	v_lshl_add_u64 v[8:9], v[4:5], 0, v[8:9]
	global_load_dwordx2 v[60:61], v[8:9], off nt
	v_or_b32_e32 v8, 0x4800, v6
	v_mov_b32_e32 v9, v7
	v_lshl_add_u64 v[8:9], v[4:5], 0, v[8:9]
	global_load_dwordx2 v[58:59], v[8:9], off nt
	v_or_b32_e32 v8, 0x4a00, v6
	v_mov_b32_e32 v9, v7
; DI unsigned pk2(float lo, float hi) { f32x2 v = {lo, hi}; bf16x2v r = __builtin_convertvector(v, bf16x2v); return __builtin_bit_cast(unsigned, r); }
; DI void phase_scan(Frame& F, int l) {
;     ...
;     for (int u = F.bid; u < NG * 2; u += F.G) { const int g = u >> 1, b = (u & 1) * 8 + (F.tid >> 6), p = F.tid & 63;
;         const float lr = l32[(g * SP + p) * 2], li = l32[(g * SP + p) * 2 + 1];
;         const size_t row0 = (size_t)g * CROWS + b * NCH; float sr = 0.f, si = 0.f;
;         f32x2 ev[NCH];
; #pragma unroll
;         for (int k = 0; k < NCH; ++k) ev[k] = *(const f32x2*)(E + (row0 + k) * 128 + 2 * p);
;         asm volatile("" ::: "memory");
; #pragma unroll
;         for (int k = 0; k < NCH; ++k) {
;             *(unsigned*)(ua + (row0 + k) * UAK + 512 + 2 * p) = pk2(sr, si);
;             const float nr = lr * sr - li * si + ev[k][0], ni = lr * si + li * sr + ev[k][1]; sr = nr; si = ni; }
	v_lshl_add_u64 v[8:9], v[4:5], 0, v[8:9]
	global_load_dwordx2 v[56:57], v[8:9], off nt
	v_or_b32_e32 v8, 0x4c00, v6
	v_mov_b32_e32 v9, v7
	v_lshl_add_u64 v[8:9], v[4:5], 0, v[8:9]
	global_load_dwordx2 v[54:55], v[8:9], off nt
	v_or_b32_e32 v8, 0x4e00, v6
	v_mov_b32_e32 v9, v7
	v_lshl_add_u64 v[8:9], v[4:5], 0, v[8:9]
	global_load_dwordx2 v[52:53], v[8:9], off nt
	v_or_b32_e32 v8, 0x5000, v6
	v_mov_b32_e32 v9, v7
	v_lshl_add_u64 v[8:9], v[4:5], 0, v[8:9]
	global_load_dwordx2 v[50:51], v[8:9], off nt
	v_or_b32_e32 v8, 0x5200, v6
	v_mov_b32_e32 v9, v7
	v_lshl_add_u64 v[8:9], v[4:5], 0, v[8:9]
	global_load_dwordx2 v[48:49], v[8:9], off nt
	v_or_b32_e32 v8, 0x5400, v6
	v_mov_b32_e32 v9, v7
	v_lshl_add_u64 v[8:9], v[4:5], 0, v[8:9]
	global_load_dwordx2 v[46:47], v[8:9], off nt
	v_or_b32_e32 v8, 0x5600, v6
	v_mov_b32_e32 v9, v7
	v_lshl_add_u64 v[8:9], v[4:5], 0, v[8:9]
	global_load_dwordx2 v[44:45], v[8:9], off nt
	v_or_b32_e32 v8, 0x5800, v6
	v_mov_b32_e32 v9, v7
	v_lshl_add_u64 v[8:9], v[4:5], 0, v[8:9]
	global_load_dwordx2 v[42:43], v[8:9], off nt
	v_or_b32_e32 v8, 0x5a00, v6
	v_mov_b32_e32 v9, v7
	v_lshl_add_u64 v[8:9], v[4:5], 0, v[8:9]
	global_load_dwordx2 v[40:41], v[8:9], off nt
	v_or_b32_e32 v8, 0x5c00, v6
	v_mov_b32_e32 v9, v7
	v_lshl_add_u64 v[8:9], v[4:5], 0, v[8:9]
	global_load_dwordx2 v[38:39], v[8:9], off nt
	v_or_b32_e32 v8, 0x5e00, v6
	v_mov_b32_e32 v9, v7
	v_lshl_add_u64 v[8:9], v[4:5], 0, v[8:9]
	global_load_dwordx2 v[36:37], v[8:9], off nt
	v_or_b32_e32 v8, 0x6000, v6
	v_mov_b32_e32 v9, v7
	v_lshl_add_u64 v[8:9], v[4:5], 0, v[8:9]
	global_load_dwordx2 v[34:35], v[8:9], off nt
	v_or_b32_e32 v8, 0x6200, v6
	v_mov_b32_e32 v9, v7
	v_lshl_add_u64 v[8:9], v[4:5], 0, v[8:9]
	global_load_dwordx2 v[32:33], v[8:9], off nt
	v_or_b32_e32 v8, 0x6400, v6
	v_mov_b32_e32 v9, v7
	v_lshl_add_u64 v[8:9], v[4:5], 0, v[8:9]
	global_load_dwordx2 v[30:31], v[8:9], off nt
	v_or_b32_e32 v8, 0x6600, v6
	v_mov_b32_e32 v9, v7
	v_lshl_add_u64 v[8:9], v[4:5], 0, v[8:9]
	global_load_dwordx2 v[28:29], v[8:9], off nt
	v_or_b32_e32 v8, 0x6800, v6
	v_mov_b32_e32 v9, v7
	v_lshl_add_u64 v[8:9], v[4:5], 0, v[8:9]
	global_load_dwordx2 v[26:27], v[8:9], off nt
	v_or_b32_e32 v8, 0x6a00, v6
	v_mov_b32_e32 v9, v7
	v_lshl_add_u64 v[8:9], v[4:5], 0, v[8:9]
	global_load_dwordx2 v[24:25], v[8:9], off nt
	v_or_b32_e32 v8, 0x6c00, v6
	v_mov_b32_e32 v9, v7
	v_lshl_add_u64 v[8:9], v[4:5], 0, v[8:9]
	global_load_dwordx2 v[22:23], v[8:9], off nt
	v_or_b32_e32 v8, 0x6e00, v6
	v_mov_b32_e32 v9, v7
	v_lshl_add_u64 v[8:9], v[4:5], 0, v[8:9]
	global_load_dwordx2 v[20:21], v[8:9], off nt
	v_or_b32_e32 v8, 0x7000, v6
	v_mov_b32_e32 v9, v7
	v_lshl_add_u64 v[8:9], v[4:5], 0, v[8:9]
	global_load_dwordx2 v[18:19], v[8:9], off nt
	v_or_b32_e32 v8, 0x7200, v6
	v_mov_b32_e32 v9, v7
	v_lshl_add_u64 v[8:9], v[4:5], 0, v[8:9]
	v_mad_u64_u32 v[136:137], s[0:1], v134, s63, v[136:137]
	global_load_dwordx2 v[16:17], v[8:9], off nt
	v_or_b32_e32 v8, 0x7400, v6
	v_mov_b32_e32 v9, v7
	v_mad_i32_i24 v137, v135, s63, v137
	v_lshlrev_b32_e32 v0, 1, v2
	v_lshl_add_u64 v[8:9], v[4:5], 0, v[8:9]
	v_lshl_add_u64 v[134:135], v[136:137], 0, v[0:1]
	s_waitcnt vmcnt(0)
	v_mul_f32_e32 v0, 0, v132
	v_mul_f32_e32 v139, 0, v133
	global_load_dwordx2 v[14:15], v[8:9], off nt
	v_or_b32_e32 v8, 0x7600, v6
	v_mov_b32_e32 v9, v7
	v_sub_f32_e32 v138, v0, v139
	v_fmac_f32_e32 v139, 0, v132
	v_lshl_add_u64 v[8:9], v[4:5], 0, v[8:9]
	v_pk_add_f32 v[130:131], v[138:139], v[130:131]
	global_load_dwordx2 v[12:13], v[8:9], off nt
	v_or_b32_e32 v8, 0x7800, v6
	v_mov_b32_e32 v9, v7
	v_pk_mul_f32 v[138:139], v[132:133], v[130:131] op_sel:[1,1] op_sel_hi:[0,1]
	v_lshl_add_u64 v[8:9], v[4:5], 0, v[8:9]
	s_mov_b32 s0, 0x28200000
	v_cvt_pk_bf16_f32 v0, v130, v131
	v_pk_fma_f32 v[140:141], v[132:133], v[130:131], v[138:139] neg_lo:[0,0,1] neg_hi:[0,0,1]
	v_pk_fma_f32 v[130:131], v[132:133], v[130:131], v[138:139] op_sel_hi:[1,0,1]
	global_load_dwordx2 v[10:11], v[8:9], off nt
	v_or_b32_e32 v8, 0x7a00, v6
	v_mov_b32_e32 v9, v7
	v_or_b32_e32 v6, 0x7c00, v6
	v_add_co_u32_e32 v136, vcc, s0, v134
	v_mov_b32_e32 v141, v131
	v_lshl_add_u64 v[8:9], v[4:5], 0, v[8:9]
	v_lshl_add_u64 v[6:7], v[4:5], 0, v[6:7]
	v_addc_co_u32_e32 v137, vcc, 0, v135, vcc
	v_pk_add_f32 v[128:129], v[128:129], v[140:141]
	global_load_dwordx2 v[8:9], v[8:9], off nt
	v_pk_mul_f32 v[130:131], v[132:133], v[128:129] op_sel:[1,1] op_sel_hi:[0,1]
	global_load_dwordx2 v[6:7], v[6:7], off nt
	global_store_dword v[136:137], v0, off offset:2304
	v_cvt_pk_bf16_f32 v0, v128, v129
	global_store_dword v[136:137], v1, off offset:1024
	global_store_dword v[136:137], v0, off offset:3584
	v_pk_fma_f32 v[136:137], v[132:133], v[128:129], v[130:131] neg_lo:[0,0,1] neg_hi:[0,0,1]
	v_pk_fma_f32 v[128:129], v[132:133], v[128:129], v[130:131] op_sel_hi:[1,0,1]
	s_mov_b32 s0, 0x28201000
	v_mov_b32_e32 v137, v129
	v_pk_add_f32 v[126:127], v[126:127], v[136:137]
	v_add_co_u32_e32 v128, vcc, s0, v134
	v_pk_mul_f32 v[130:131], v[132:133], v[126:127] op_sel:[1,1] op_sel_hi:[0,1]
	v_cvt_pk_bf16_f32 v0, v126, v127
	v_pk_fma_f32 v[136:137], v[132:133], v[126:127], v[130:131] neg_lo:[0,0,1] neg_hi:[0,0,1]
	v_pk_fma_f32 v[126:127], v[132:133], v[126:127], v[130:131] op_sel_hi:[1,0,1]
	v_addc_co_u32_e32 v129, vcc, 0, v135, vcc
	v_mov_b32_e32 v137, v127
	v_pk_add_f32 v[124:125], v[124:125], v[136:137]
	global_store_dword v[128:129], v0, off offset:768
	v_pk_mul_f32 v[126:127], v[132:133], v[124:125] op_sel:[1,1] op_sel_hi:[0,1]
	v_cvt_pk_bf16_f32 v0, v124, v125
	v_pk_fma_f32 v[130:131], v[132:133], v[124:125], v[126:127] neg_lo:[0,0,1] neg_hi:[0,0,1]
	v_pk_fma_f32 v[124:125], v[132:133], v[124:125], v[126:127] op_sel_hi:[1,0,1]
; DI unsigned pk2(float lo, float hi) { f32x2 v = {lo, hi}; bf16x2v r = __builtin_convertvector(v, bf16x2v); return __builtin_bit_cast(unsigned, r); }
; DI void phase_scan(Frame& F, int l) {
;     ...
; #pragma unroll
;         for (int k = 0; k < NCH; ++k) {
;             *(unsigned*)(ua + (row0 + k) * UAK + 512 + 2 * p) = pk2(sr, si);
;             const float nr = lr * sr - li * si + ev[k][0], ni = lr * si + li * sr + ev[k][1]; sr = nr; si = ni; }
	global_store_dword v[128:129], v0, off offset:2048
	v_mov_b32_e32 v131, v125
	v_pk_add_f32 v[122:123], v[122:123], v[130:131]
	s_mov_b32 s0, 0x28202000
	v_pk_mul_f32 v[124:125], v[132:133], v[122:123] op_sel:[1,1] op_sel_hi:[0,1]
	v_cvt_pk_bf16_f32 v0, v122, v123
	v_pk_fma_f32 v[126:127], v[132:133], v[122:123], v[124:125] neg_lo:[0,0,1] neg_hi:[0,0,1]
	v_pk_fma_f32 v[122:123], v[132:133], v[122:123], v[124:125] op_sel_hi:[1,0,1]
	global_store_dword v[128:129], v0, off offset:3328
	v_mov_b32_e32 v127, v123
	v_pk_add_f32 v[120:121], v[120:121], v[126:127]
	v_add_co_u32_e32 v122, vcc, s0, v134
	v_pk_mul_f32 v[124:125], v[132:133], v[120:121] op_sel:[1,1] op_sel_hi:[0,1]
	v_cvt_pk_bf16_f32 v0, v120, v121
	v_pk_fma_f32 v[126:127], v[132:133], v[120:121], v[124:125] neg_lo:[0,0,1] neg_hi:[0,0,1]
	v_pk_fma_f32 v[120:121], v[132:133], v[120:121], v[124:125] op_sel_hi:[1,0,1]
	v_addc_co_u32_e32 v123, vcc, 0, v135, vcc
	v_mov_b32_e32 v127, v121
	v_pk_add_f32 v[118:119], v[118:119], v[126:127]
	global_store_dword v[122:123], v0, off offset:512
	v_pk_mul_f32 v[120:121], v[132:133], v[118:119] op_sel:[1,1] op_sel_hi:[0,1]
	v_cvt_pk_bf16_f32 v0, v118, v119
	v_pk_fma_f32 v[124:125], v[132:133], v[118:119], v[120:121] neg_lo:[0,0,1] neg_hi:[0,0,1]
	v_pk_fma_f32 v[118:119], v[132:133], v[118:119], v[120:121] op_sel_hi:[1,0,1]
	global_store_dword v[122:123], v0, off offset:1792
	v_mov_b32_e32 v125, v119
	v_pk_add_f32 v[116:117], v[116:117], v[124:125]
	s_mov_b32 s0, 0x28203000
	v_pk_mul_f32 v[118:119], v[132:133], v[116:117] op_sel:[1,1] op_sel_hi:[0,1]
	v_cvt_pk_bf16_f32 v0, v116, v117
	v_pk_fma_f32 v[120:121], v[132:133], v[116:117], v[118:119] neg_lo:[0,0,1] neg_hi:[0,0,1]
	v_pk_fma_f32 v[116:117], v[132:133], v[116:117], v[118:119] op_sel_hi:[1,0,1]
	global_store_dword v[122:123], v0, off offset:3072
	v_mov_b32_e32 v121, v117
	v_pk_add_f32 v[114:115], v[114:115], v[120:121]
	v_add_co_u32_e32 v116, vcc, s0, v134
	v_pk_mul_f32 v[118:119], v[132:133], v[114:115] op_sel:[1,1] op_sel_hi:[0,1]
	v_cvt_pk_bf16_f32 v0, v114, v115
	v_pk_fma_f32 v[120:121], v[132:133], v[114:115], v[118:119] neg_lo:[0,0,1] neg_hi:[0,0,1]
	v_pk_fma_f32 v[114:115], v[132:133], v[114:115], v[118:119] op_sel_hi:[1,0,1]
	v_addc_co_u32_e32 v117, vcc, 0, v135, vcc
	v_mov_b32_e32 v121, v115
	v_pk_add_f32 v[112:113], v[112:113], v[120:121]
	global_store_dword v[116:117], v0, off offset:256
	v_pk_mul_f32 v[114:115], v[132:133], v[112:113] op_sel:[1,1] op_sel_hi:[0,1]
	v_cvt_pk_bf16_f32 v0, v112, v113
	v_pk_fma_f32 v[118:119], v[132:133], v[112:113], v[114:115] neg_lo:[0,0,1] neg_hi:[0,0,1]
	v_pk_fma_f32 v[112:113], v[132:133], v[112:113], v[114:115] op_sel_hi:[1,0,1]
	global_store_dword v[116:117], v0, off offset:1536
	v_mov_b32_e32 v119, v113
	v_pk_add_f32 v[110:111], v[110:111], v[118:119]
	s_mov_b32 s0, 0x28204000
	v_pk_mul_f32 v[112:113], v[132:133], v[110:111] op_sel:[1,1] op_sel_hi:[0,1]
	v_cvt_pk_bf16_f32 v0, v110, v111
	v_pk_fma_f32 v[114:115], v[132:133], v[110:111], v[112:113] neg_lo:[0,0,1] neg_hi:[0,0,1]
	v_pk_fma_f32 v[110:111], v[132:133], v[110:111], v[112:113] op_sel_hi:[1,0,1]
	global_store_dword v[116:117], v0, off offset:2816
	v_mov_b32_e32 v115, v111
	v_pk_add_f32 v[108:109], v[108:109], v[114:115]
	v_add_co_u32_e32 v110, vcc, s0, v134
	v_pk_mul_f32 v[112:113], v[132:133], v[108:109] op_sel:[1,1] op_sel_hi:[0,1]
	v_cvt_pk_bf16_f32 v0, v108, v109
	v_pk_fma_f32 v[114:115], v[132:133], v[108:109], v[112:113] neg_lo:[0,0,1] neg_hi:[0,0,1]
	v_pk_fma_f32 v[108:109], v[132:133], v[108:109], v[112:113] op_sel_hi:[1,0,1]
	v_addc_co_u32_e32 v111, vcc, 0, v135, vcc
	v_mov_b32_e32 v115, v109
	v_pk_add_f32 v[106:107], v[106:107], v[114:115]
	global_store_dword v[110:111], v0, off
	v_pk_mul_f32 v[108:109], v[132:133], v[106:107] op_sel:[1,1] op_sel_hi:[0,1]
	v_cvt_pk_bf16_f32 v0, v106, v107
	v_pk_fma_f32 v[112:113], v[132:133], v[106:107], v[108:109] neg_lo:[0,0,1] neg_hi:[0,0,1]
	v_pk_fma_f32 v[106:107], v[132:133], v[106:107], v[108:109] op_sel_hi:[1,0,1]
	global_store_dword v[110:111], v0, off offset:1280
	v_mov_b32_e32 v113, v107
	v_pk_add_f32 v[104:105], v[104:105], v[112:113]
	s_mov_b32 s0, 0x28205000
	v_pk_mul_f32 v[106:107], v[132:133], v[104:105] op_sel:[1,1] op_sel_hi:[0,1]
	v_cvt_pk_bf16_f32 v0, v104, v105
	v_pk_fma_f32 v[108:109], v[132:133], v[104:105], v[106:107] neg_lo:[0,0,1] neg_hi:[0,0,1]
	v_pk_fma_f32 v[104:105], v[132:133], v[104:105], v[106:107] op_sel_hi:[1,0,1]
	global_store_dword v[110:111], v0, off offset:2560
	v_mov_b32_e32 v109, v105
	v_pk_add_f32 v[102:103], v[102:103], v[108:109]
	s_add_i32 s2, s2, s72
	v_pk_mul_f32 v[104:105], v[132:133], v[102:103] op_sel:[1,1] op_sel_hi:[0,1]
	v_cvt_pk_bf16_f32 v0, v102, v103
	v_pk_fma_f32 v[106:107], v[132:133], v[102:103], v[104:105] neg_lo:[0,0,1] neg_hi:[0,0,1]
	v_pk_fma_f32 v[102:103], v[132:133], v[102:103], v[104:105] op_sel_hi:[1,0,1]
	global_store_dword v[110:111], v0, off offset:3840
	v_mov_b32_e32 v107, v103
	v_pk_add_f32 v[100:101], v[100:101], v[106:107]
	v_add_co_u32_e32 v102, vcc, s0, v134
	v_pk_mul_f32 v[104:105], v[132:133], v[100:101] op_sel:[1,1] op_sel_hi:[0,1]
	v_cvt_pk_bf16_f32 v0, v100, v101
	v_pk_fma_f32 v[106:107], v[132:133], v[100:101], v[104:105] neg_lo:[0,0,1] neg_hi:[0,0,1]
	v_pk_fma_f32 v[100:101], v[132:133], v[100:101], v[104:105] op_sel_hi:[1,0,1]
	v_addc_co_u32_e32 v103, vcc, 0, v135, vcc
	v_mov_b32_e32 v107, v101
	v_pk_add_f32 v[98:99], v[98:99], v[106:107]
	global_store_dword v[102:103], v0, off offset:1024
	v_pk_mul_f32 v[100:101], v[132:133], v[98:99] op_sel:[1,1] op_sel_hi:[0,1]
	v_cvt_pk_bf16_f32 v0, v98, v99
	v_pk_fma_f32 v[104:105], v[132:133], v[98:99], v[100:101] neg_lo:[0,0,1] neg_hi:[0,0,1]
; DI unsigned pk2(float lo, float hi) { f32x2 v = {lo, hi}; bf16x2v r = __builtin_convertvector(v, bf16x2v); return __builtin_bit_cast(unsigned, r); }
; DI void phase_scan(Frame& F, int l) {
;     ...
; #pragma unroll
;         for (int k = 0; k < NCH; ++k) {
;             *(unsigned*)(ua + (row0 + k) * UAK + 512 + 2 * p) = pk2(sr, si);
;             const float nr = lr * sr - li * si + ev[k][0], ni = lr * si + li * sr + ev[k][1]; sr = nr; si = ni; }
	v_pk_fma_f32 v[98:99], v[132:133], v[98:99], v[100:101] op_sel_hi:[1,0,1]
	global_store_dword v[102:103], v0, off offset:2304
	v_mov_b32_e32 v105, v99
	v_pk_add_f32 v[96:97], v[96:97], v[104:105]
	s_mov_b32 s0, 0x28206000
	v_pk_mul_f32 v[98:99], v[132:133], v[96:97] op_sel:[1,1] op_sel_hi:[0,1]
	v_cvt_pk_bf16_f32 v0, v96, v97
	v_pk_fma_f32 v[100:101], v[132:133], v[96:97], v[98:99] neg_lo:[0,0,1] neg_hi:[0,0,1]
	v_pk_fma_f32 v[96:97], v[132:133], v[96:97], v[98:99] op_sel_hi:[1,0,1]
	global_store_dword v[102:103], v0, off offset:3584
	v_mov_b32_e32 v101, v97
	v_pk_add_f32 v[94:95], v[94:95], v[100:101]
	v_add_co_u32_e32 v96, vcc, s0, v134
	v_pk_mul_f32 v[98:99], v[132:133], v[94:95] op_sel:[1,1] op_sel_hi:[0,1]
	v_cvt_pk_bf16_f32 v0, v94, v95
	v_pk_fma_f32 v[100:101], v[132:133], v[94:95], v[98:99] neg_lo:[0,0,1] neg_hi:[0,0,1]
	v_pk_fma_f32 v[94:95], v[132:133], v[94:95], v[98:99] op_sel_hi:[1,0,1]
	v_addc_co_u32_e32 v97, vcc, 0, v135, vcc
	v_mov_b32_e32 v101, v95
	v_pk_add_f32 v[92:93], v[92:93], v[100:101]
	global_store_dword v[96:97], v0, off offset:768
	v_pk_mul_f32 v[94:95], v[132:133], v[92:93] op_sel:[1,1] op_sel_hi:[0,1]
	v_cvt_pk_bf16_f32 v0, v92, v93
	v_pk_fma_f32 v[98:99], v[132:133], v[92:93], v[94:95] neg_lo:[0,0,1] neg_hi:[0,0,1]
	v_pk_fma_f32 v[92:93], v[132:133], v[92:93], v[94:95] op_sel_hi:[1,0,1]
	global_store_dword v[96:97], v0, off offset:2048
	v_mov_b32_e32 v99, v93
	v_pk_add_f32 v[90:91], v[90:91], v[98:99]
	s_mov_b32 s0, 0x28207000
	v_pk_mul_f32 v[92:93], v[132:133], v[90:91] op_sel:[1,1] op_sel_hi:[0,1]
	v_cvt_pk_bf16_f32 v0, v90, v91
	v_pk_fma_f32 v[94:95], v[132:133], v[90:91], v[92:93] neg_lo:[0,0,1] neg_hi:[0,0,1]
	v_pk_fma_f32 v[90:91], v[132:133], v[90:91], v[92:93] op_sel_hi:[1,0,1]
	global_store_dword v[96:97], v0, off offset:3328
	v_mov_b32_e32 v95, v91
	v_pk_add_f32 v[88:89], v[88:89], v[94:95]
	v_add_co_u32_e32 v90, vcc, s0, v134
	v_pk_mul_f32 v[92:93], v[132:133], v[88:89] op_sel:[1,1] op_sel_hi:[0,1]
	v_cvt_pk_bf16_f32 v0, v88, v89
	v_pk_fma_f32 v[94:95], v[132:133], v[88:89], v[92:93] neg_lo:[0,0,1] neg_hi:[0,0,1]
	v_pk_fma_f32 v[88:89], v[132:133], v[88:89], v[92:93] op_sel_hi:[1,0,1]
	v_addc_co_u32_e32 v91, vcc, 0, v135, vcc
	v_mov_b32_e32 v95, v89
	v_pk_add_f32 v[86:87], v[86:87], v[94:95]
	global_store_dword v[90:91], v0, off offset:512
	v_pk_mul_f32 v[88:89], v[132:133], v[86:87] op_sel:[1,1] op_sel_hi:[0,1]
	v_cvt_pk_bf16_f32 v0, v86, v87
	v_pk_fma_f32 v[92:93], v[132:133], v[86:87], v[88:89] neg_lo:[0,0,1] neg_hi:[0,0,1]
	v_pk_fma_f32 v[86:87], v[132:133], v[86:87], v[88:89] op_sel_hi:[1,0,1]
	global_store_dword v[90:91], v0, off offset:1792
	v_mov_b32_e32 v93, v87
	v_pk_add_f32 v[84:85], v[84:85], v[92:93]
	s_mov_b32 s0, 0x28208000
	v_pk_mul_f32 v[86:87], v[132:133], v[84:85] op_sel:[1,1] op_sel_hi:[0,1]
	v_cvt_pk_bf16_f32 v0, v84, v85
	v_pk_fma_f32 v[88:89], v[132:133], v[84:85], v[86:87] neg_lo:[0,0,1] neg_hi:[0,0,1]
	v_pk_fma_f32 v[84:85], v[132:133], v[84:85], v[86:87] op_sel_hi:[1,0,1]
	global_store_dword v[90:91], v0, off offset:3072
	v_mov_b32_e32 v89, v85
	v_pk_add_f32 v[82:83], v[82:83], v[88:89]
	v_add_co_u32_e32 v84, vcc, s0, v134
	v_pk_mul_f32 v[86:87], v[132:133], v[82:83] op_sel:[1,1] op_sel_hi:[0,1]
	v_cvt_pk_bf16_f32 v0, v82, v83
	v_pk_fma_f32 v[88:89], v[132:133], v[82:83], v[86:87] neg_lo:[0,0,1] neg_hi:[0,0,1]
	v_pk_fma_f32 v[82:83], v[132:133], v[82:83], v[86:87] op_sel_hi:[1,0,1]
	v_addc_co_u32_e32 v85, vcc, 0, v135, vcc
	v_mov_b32_e32 v89, v83
	v_pk_add_f32 v[80:81], v[80:81], v[88:89]
	global_store_dword v[84:85], v0, off offset:256
	v_pk_mul_f32 v[82:83], v[132:133], v[80:81] op_sel:[1,1] op_sel_hi:[0,1]
	v_cvt_pk_bf16_f32 v0, v80, v81
	v_pk_fma_f32 v[86:87], v[132:133], v[80:81], v[82:83] neg_lo:[0,0,1] neg_hi:[0,0,1]
	v_pk_fma_f32 v[80:81], v[132:133], v[80:81], v[82:83] op_sel_hi:[1,0,1]
	global_store_dword v[84:85], v0, off offset:1536
	v_mov_b32_e32 v87, v81
	v_pk_add_f32 v[78:79], v[78:79], v[86:87]
	s_mov_b32 s0, 0x28209000
	v_pk_mul_f32 v[80:81], v[132:133], v[78:79] op_sel:[1,1] op_sel_hi:[0,1]
	v_cvt_pk_bf16_f32 v0, v78, v79
	v_pk_fma_f32 v[82:83], v[132:133], v[78:79], v[80:81] neg_lo:[0,0,1] neg_hi:[0,0,1]
	v_pk_fma_f32 v[78:79], v[132:133], v[78:79], v[80:81] op_sel_hi:[1,0,1]
	global_store_dword v[84:85], v0, off offset:2816
	v_mov_b32_e32 v83, v79
	v_pk_add_f32 v[76:77], v[76:77], v[82:83]
	v_add_co_u32_e32 v78, vcc, s0, v134
	v_pk_mul_f32 v[80:81], v[132:133], v[76:77] op_sel:[1,1] op_sel_hi:[0,1]
	v_cvt_pk_bf16_f32 v0, v76, v77
	v_pk_fma_f32 v[82:83], v[132:133], v[76:77], v[80:81] neg_lo:[0,0,1] neg_hi:[0,0,1]
	v_pk_fma_f32 v[76:77], v[132:133], v[76:77], v[80:81] op_sel_hi:[1,0,1]
	v_addc_co_u32_e32 v79, vcc, 0, v135, vcc
	v_mov_b32_e32 v83, v77
	v_pk_add_f32 v[74:75], v[74:75], v[82:83]
	global_store_dword v[78:79], v0, off
	v_pk_mul_f32 v[76:77], v[132:133], v[74:75] op_sel:[1,1] op_sel_hi:[0,1]
	v_cvt_pk_bf16_f32 v0, v74, v75
	v_pk_fma_f32 v[80:81], v[132:133], v[74:75], v[76:77] neg_lo:[0,0,1] neg_hi:[0,0,1]
	v_pk_fma_f32 v[74:75], v[132:133], v[74:75], v[76:77] op_sel_hi:[1,0,1]
	global_store_dword v[78:79], v0, off offset:1280
	v_mov_b32_e32 v81, v75
	v_pk_add_f32 v[72:73], v[72:73], v[80:81]
	s_mov_b32 s0, 0x2820a000
	v_pk_mul_f32 v[74:75], v[132:133], v[72:73] op_sel:[1,1] op_sel_hi:[0,1]
	v_cvt_pk_bf16_f32 v0, v72, v73
	v_pk_fma_f32 v[76:77], v[132:133], v[72:73], v[74:75] neg_lo:[0,0,1] neg_hi:[0,0,1]
	v_pk_fma_f32 v[72:73], v[132:133], v[72:73], v[74:75] op_sel_hi:[1,0,1]
	global_store_dword v[78:79], v0, off offset:2560
	v_mov_b32_e32 v77, v73
	v_pk_add_f32 v[70:71], v[70:71], v[76:77]
	s_add_i32 s3, s3, s55
; DI unsigned pk2(float lo, float hi) { f32x2 v = {lo, hi}; bf16x2v r = __builtin_convertvector(v, bf16x2v); return __builtin_bit_cast(unsigned, r); }
; DI void phase_scan(Frame& F, int l) {
;     ...
; #pragma unroll
;         for (int k = 0; k < NCH; ++k) {
;             *(unsigned*)(ua + (row0 + k) * UAK + 512 + 2 * p) = pk2(sr, si);
;             const float nr = lr * sr - li * si + ev[k][0], ni = lr * si + li * sr + ev[k][1]; sr = nr; si = ni; }
	v_pk_mul_f32 v[72:73], v[132:133], v[70:71] op_sel:[1,1] op_sel_hi:[0,1]
	v_cvt_pk_bf16_f32 v0, v70, v71
	v_pk_fma_f32 v[74:75], v[132:133], v[70:71], v[72:73] neg_lo:[0,0,1] neg_hi:[0,0,1]
	v_pk_fma_f32 v[70:71], v[132:133], v[70:71], v[72:73] op_sel_hi:[1,0,1]
	global_store_dword v[78:79], v0, off offset:3840
	v_mov_b32_e32 v75, v71
	v_pk_add_f32 v[68:69], v[68:69], v[74:75]
	v_add_co_u32_e32 v70, vcc, s0, v134
	v_pk_mul_f32 v[72:73], v[132:133], v[68:69] op_sel:[1,1] op_sel_hi:[0,1]
	v_cvt_pk_bf16_f32 v0, v68, v69
	v_pk_fma_f32 v[74:75], v[132:133], v[68:69], v[72:73] neg_lo:[0,0,1] neg_hi:[0,0,1]
	v_pk_fma_f32 v[68:69], v[132:133], v[68:69], v[72:73] op_sel_hi:[1,0,1]
	v_addc_co_u32_e32 v71, vcc, 0, v135, vcc
	v_mov_b32_e32 v75, v69
	v_pk_add_f32 v[66:67], v[66:67], v[74:75]
	global_store_dword v[70:71], v0, off offset:1024
	v_pk_mul_f32 v[68:69], v[132:133], v[66:67] op_sel:[1,1] op_sel_hi:[0,1]
	v_cvt_pk_bf16_f32 v0, v66, v67
	v_pk_fma_f32 v[72:73], v[132:133], v[66:67], v[68:69] neg_lo:[0,0,1] neg_hi:[0,0,1]
	v_pk_fma_f32 v[66:67], v[132:133], v[66:67], v[68:69] op_sel_hi:[1,0,1]
	global_store_dword v[70:71], v0, off offset:2304
	v_mov_b32_e32 v73, v67
	v_pk_add_f32 v[64:65], v[64:65], v[72:73]
	s_mov_b32 s0, 0x2820b000
	v_pk_mul_f32 v[66:67], v[132:133], v[64:65] op_sel:[1,1] op_sel_hi:[0,1]
	v_cvt_pk_bf16_f32 v0, v64, v65
	v_pk_fma_f32 v[68:69], v[132:133], v[64:65], v[66:67] neg_lo:[0,0,1] neg_hi:[0,0,1]
	v_pk_fma_f32 v[64:65], v[132:133], v[64:65], v[66:67] op_sel_hi:[1,0,1]
	global_store_dword v[70:71], v0, off offset:3584
	v_mov_b32_e32 v69, v65
	v_pk_add_f32 v[62:63], v[62:63], v[68:69]
	v_add_co_u32_e32 v64, vcc, s0, v134
	v_pk_mul_f32 v[66:67], v[132:133], v[62:63] op_sel:[1,1] op_sel_hi:[0,1]
	v_cvt_pk_bf16_f32 v0, v62, v63
	v_pk_fma_f32 v[68:69], v[132:133], v[62:63], v[66:67] neg_lo:[0,0,1] neg_hi:[0,0,1]
	v_pk_fma_f32 v[62:63], v[132:133], v[62:63], v[66:67] op_sel_hi:[1,0,1]
	v_addc_co_u32_e32 v65, vcc, 0, v135, vcc
	v_mov_b32_e32 v69, v63
	v_pk_add_f32 v[60:61], v[60:61], v[68:69]
	global_store_dword v[64:65], v0, off offset:768
	v_pk_mul_f32 v[62:63], v[132:133], v[60:61] op_sel:[1,1] op_sel_hi:[0,1]
	v_cvt_pk_bf16_f32 v0, v60, v61
	v_pk_fma_f32 v[66:67], v[132:133], v[60:61], v[62:63] neg_lo:[0,0,1] neg_hi:[0,0,1]
	v_pk_fma_f32 v[60:61], v[132:133], v[60:61], v[62:63] op_sel_hi:[1,0,1]
	global_store_dword v[64:65], v0, off offset:2048
	v_mov_b32_e32 v67, v61
	v_pk_add_f32 v[58:59], v[58:59], v[66:67]
	s_mov_b32 s0, 0x2820c000
	v_pk_mul_f32 v[60:61], v[132:133], v[58:59] op_sel:[1,1] op_sel_hi:[0,1]
	v_cvt_pk_bf16_f32 v0, v58, v59
	v_pk_fma_f32 v[62:63], v[132:133], v[58:59], v[60:61] neg_lo:[0,0,1] neg_hi:[0,0,1]
	v_pk_fma_f32 v[58:59], v[132:133], v[58:59], v[60:61] op_sel_hi:[1,0,1]
	global_store_dword v[64:65], v0, off offset:3328
	v_mov_b32_e32 v63, v59
	v_pk_add_f32 v[56:57], v[56:57], v[62:63]
	v_add_co_u32_e32 v58, vcc, s0, v134
	v_pk_mul_f32 v[60:61], v[132:133], v[56:57] op_sel:[1,1] op_sel_hi:[0,1]
	v_cvt_pk_bf16_f32 v0, v56, v57
	v_pk_fma_f32 v[62:63], v[132:133], v[56:57], v[60:61] neg_lo:[0,0,1] neg_hi:[0,0,1]
	v_pk_fma_f32 v[56:57], v[132:133], v[56:57], v[60:61] op_sel_hi:[1,0,1]
	v_addc_co_u32_e32 v59, vcc, 0, v135, vcc
	v_mov_b32_e32 v63, v57
	v_pk_add_f32 v[54:55], v[54:55], v[62:63]
	global_store_dword v[58:59], v0, off offset:512
	v_pk_mul_f32 v[56:57], v[132:133], v[54:55] op_sel:[1,1] op_sel_hi:[0,1]
	v_cvt_pk_bf16_f32 v0, v54, v55
	v_pk_fma_f32 v[60:61], v[132:133], v[54:55], v[56:57] neg_lo:[0,0,1] neg_hi:[0,0,1]
	v_pk_fma_f32 v[54:55], v[132:133], v[54:55], v[56:57] op_sel_hi:[1,0,1]
	global_store_dword v[58:59], v0, off offset:1792
	v_mov_b32_e32 v61, v55
	v_pk_add_f32 v[52:53], v[52:53], v[60:61]
	s_mov_b32 s0, 0x2820d000
	v_pk_mul_f32 v[54:55], v[132:133], v[52:53] op_sel:[1,1] op_sel_hi:[0,1]
	v_cvt_pk_bf16_f32 v0, v52, v53
	v_pk_fma_f32 v[56:57], v[132:133], v[52:53], v[54:55] neg_lo:[0,0,1] neg_hi:[0,0,1]
	v_pk_fma_f32 v[52:53], v[132:133], v[52:53], v[54:55] op_sel_hi:[1,0,1]
	global_store_dword v[58:59], v0, off offset:3072
	v_mov_b32_e32 v57, v53
	v_pk_add_f32 v[50:51], v[50:51], v[56:57]
	v_add_co_u32_e32 v52, vcc, s0, v134
	v_pk_mul_f32 v[54:55], v[132:133], v[50:51] op_sel:[1,1] op_sel_hi:[0,1]
	v_cvt_pk_bf16_f32 v0, v50, v51
	v_pk_fma_f32 v[56:57], v[132:133], v[50:51], v[54:55] neg_lo:[0,0,1] neg_hi:[0,0,1]
	v_pk_fma_f32 v[50:51], v[132:133], v[50:51], v[54:55] op_sel_hi:[1,0,1]
	v_addc_co_u32_e32 v53, vcc, 0, v135, vcc
	v_mov_b32_e32 v57, v51
	v_pk_add_f32 v[48:49], v[48:49], v[56:57]
	global_store_dword v[52:53], v0, off offset:256
	v_pk_mul_f32 v[50:51], v[132:133], v[48:49] op_sel:[1,1] op_sel_hi:[0,1]
	v_cvt_pk_bf16_f32 v0, v48, v49
	v_pk_fma_f32 v[54:55], v[132:133], v[48:49], v[50:51] neg_lo:[0,0,1] neg_hi:[0,0,1]
	v_pk_fma_f32 v[48:49], v[132:133], v[48:49], v[50:51] op_sel_hi:[1,0,1]
	global_store_dword v[52:53], v0, off offset:1536
	v_mov_b32_e32 v55, v49
	v_pk_add_f32 v[46:47], v[46:47], v[54:55]
	s_mov_b32 s0, 0x2820e000
	v_pk_mul_f32 v[48:49], v[132:133], v[46:47] op_sel:[1,1] op_sel_hi:[0,1]
	v_cvt_pk_bf16_f32 v0, v46, v47
	v_pk_fma_f32 v[50:51], v[132:133], v[46:47], v[48:49] neg_lo:[0,0,1] neg_hi:[0,0,1]
	v_pk_fma_f32 v[46:47], v[132:133], v[46:47], v[48:49] op_sel_hi:[1,0,1]
	global_store_dword v[52:53], v0, off offset:2816
	v_mov_b32_e32 v51, v47
	v_pk_add_f32 v[44:45], v[44:45], v[50:51]
	v_add_co_u32_e32 v46, vcc, s0, v134
	v_pk_mul_f32 v[48:49], v[132:133], v[44:45] op_sel:[1,1] op_sel_hi:[0,1]
	v_cvt_pk_bf16_f32 v0, v44, v45
	v_pk_fma_f32 v[50:51], v[132:133], v[44:45], v[48:49] neg_lo:[0,0,1] neg_hi:[0,0,1]
	v_pk_fma_f32 v[44:45], v[132:133], v[44:45], v[48:49] op_sel_hi:[1,0,1]
; DI unsigned pk2(float lo, float hi) { f32x2 v = {lo, hi}; bf16x2v r = __builtin_convertvector(v, bf16x2v); return __builtin_bit_cast(unsigned, r); }
; DI void phase_scan(Frame& F, int l) {
;     ...
;     for (int u = F.bid; u < NG * 2; u += F.G) { const int g = u >> 1, b = (u & 1) * 8 + (F.tid >> 6), p = F.tid & 63;
;         const float lr = l32[(g * SP + p) * 2], li = l32[(g * SP + p) * 2 + 1];
;         const size_t row0 = (size_t)g * CROWS + b * NCH; float sr = 0.f, si = 0.f;
;         f32x2 ev[NCH];
; #pragma unroll
;         for (int k = 0; k < NCH; ++k) ev[k] = *(const f32x2*)(E + (row0 + k) * 128 + 2 * p);
;         asm volatile("" ::: "memory");
; #pragma unroll
;         for (int k = 0; k < NCH; ++k) {
;             *(unsigned*)(ua + (row0 + k) * UAK + 512 + 2 * p) = pk2(sr, si);
;             const float nr = lr * sr - li * si + ev[k][0], ni = lr * si + li * sr + ev[k][1]; sr = nr; si = ni; }
;     }
	v_addc_co_u32_e32 v47, vcc, 0, v135, vcc
	v_mov_b32_e32 v51, v45
	v_pk_add_f32 v[42:43], v[42:43], v[50:51]
	global_store_dword v[46:47], v0, off
	v_pk_mul_f32 v[44:45], v[132:133], v[42:43] op_sel:[1,1] op_sel_hi:[0,1]
	v_cvt_pk_bf16_f32 v0, v42, v43
	v_pk_fma_f32 v[48:49], v[132:133], v[42:43], v[44:45] neg_lo:[0,0,1] neg_hi:[0,0,1]
	v_pk_fma_f32 v[42:43], v[132:133], v[42:43], v[44:45] op_sel_hi:[1,0,1]
	global_store_dword v[46:47], v0, off offset:1280
	v_mov_b32_e32 v49, v43
	v_pk_add_f32 v[40:41], v[40:41], v[48:49]
	s_mov_b32 s0, 0x2820f000
	v_pk_mul_f32 v[42:43], v[132:133], v[40:41] op_sel:[1,1] op_sel_hi:[0,1]
	v_cvt_pk_bf16_f32 v0, v40, v41
	v_pk_fma_f32 v[44:45], v[132:133], v[40:41], v[42:43] neg_lo:[0,0,1] neg_hi:[0,0,1]
	v_pk_fma_f32 v[40:41], v[132:133], v[40:41], v[42:43] op_sel_hi:[1,0,1]
	global_store_dword v[46:47], v0, off offset:2560
	v_mov_b32_e32 v45, v41
	v_pk_add_f32 v[38:39], v[38:39], v[44:45]
	s_cmp_lt_i32 s2, 64
	v_pk_mul_f32 v[40:41], v[132:133], v[38:39] op_sel:[1,1] op_sel_hi:[0,1]
	v_cvt_pk_bf16_f32 v0, v38, v39
	v_pk_fma_f32 v[42:43], v[132:133], v[38:39], v[40:41] neg_lo:[0,0,1] neg_hi:[0,0,1]
	v_pk_fma_f32 v[38:39], v[132:133], v[38:39], v[40:41] op_sel_hi:[1,0,1]
	global_store_dword v[46:47], v0, off offset:3840
	v_mov_b32_e32 v43, v39
	v_pk_add_f32 v[36:37], v[36:37], v[42:43]
	v_add_co_u32_e32 v38, vcc, s0, v134
	v_pk_mul_f32 v[40:41], v[132:133], v[36:37] op_sel:[1,1] op_sel_hi:[0,1]
	v_cvt_pk_bf16_f32 v0, v36, v37
	v_pk_fma_f32 v[42:43], v[132:133], v[36:37], v[40:41] neg_lo:[0,0,1] neg_hi:[0,0,1]
	v_pk_fma_f32 v[36:37], v[132:133], v[36:37], v[40:41] op_sel_hi:[1,0,1]
	v_addc_co_u32_e32 v39, vcc, 0, v135, vcc
	v_mov_b32_e32 v43, v37
	v_pk_add_f32 v[34:35], v[34:35], v[42:43]
	global_store_dword v[38:39], v0, off offset:1024
	v_pk_mul_f32 v[36:37], v[132:133], v[34:35] op_sel:[1,1] op_sel_hi:[0,1]
	v_cvt_pk_bf16_f32 v0, v34, v35
	v_pk_fma_f32 v[40:41], v[132:133], v[34:35], v[36:37] neg_lo:[0,0,1] neg_hi:[0,0,1]
	v_pk_fma_f32 v[34:35], v[132:133], v[34:35], v[36:37] op_sel_hi:[1,0,1]
	global_store_dword v[38:39], v0, off offset:2304
	v_mov_b32_e32 v41, v35
	v_pk_add_f32 v[32:33], v[32:33], v[40:41]
	s_mov_b32 s0, 0x28210000
	v_pk_mul_f32 v[34:35], v[132:133], v[32:33] op_sel:[1,1] op_sel_hi:[0,1]
	v_cvt_pk_bf16_f32 v0, v32, v33
	v_pk_fma_f32 v[36:37], v[132:133], v[32:33], v[34:35] neg_lo:[0,0,1] neg_hi:[0,0,1]
	v_pk_fma_f32 v[32:33], v[132:133], v[32:33], v[34:35] op_sel_hi:[1,0,1]
	global_store_dword v[38:39], v0, off offset:3584
	v_mov_b32_e32 v37, v33
	v_pk_add_f32 v[30:31], v[30:31], v[36:37]
	v_add_co_u32_e32 v32, vcc, s0, v134
	v_pk_mul_f32 v[34:35], v[132:133], v[30:31] op_sel:[1,1] op_sel_hi:[0,1]
	v_cvt_pk_bf16_f32 v0, v30, v31
	v_pk_fma_f32 v[36:37], v[132:133], v[30:31], v[34:35] neg_lo:[0,0,1] neg_hi:[0,0,1]
	v_pk_fma_f32 v[30:31], v[132:133], v[30:31], v[34:35] op_sel_hi:[1,0,1]
	v_addc_co_u32_e32 v33, vcc, 0, v135, vcc
	v_mov_b32_e32 v37, v31
	v_pk_add_f32 v[28:29], v[28:29], v[36:37]
	global_store_dword v[32:33], v0, off offset:768
	v_pk_mul_f32 v[30:31], v[132:133], v[28:29] op_sel:[1,1] op_sel_hi:[0,1]
	v_cvt_pk_bf16_f32 v0, v28, v29
	v_pk_fma_f32 v[34:35], v[132:133], v[28:29], v[30:31] neg_lo:[0,0,1] neg_hi:[0,0,1]
	v_pk_fma_f32 v[28:29], v[132:133], v[28:29], v[30:31] op_sel_hi:[1,0,1]
	global_store_dword v[32:33], v0, off offset:2048
	v_mov_b32_e32 v35, v29
	v_pk_add_f32 v[26:27], v[26:27], v[34:35]
	s_mov_b32 s0, 0x28211000
	v_pk_mul_f32 v[28:29], v[132:133], v[26:27] op_sel:[1,1] op_sel_hi:[0,1]
	v_cvt_pk_bf16_f32 v0, v26, v27
	v_pk_fma_f32 v[30:31], v[132:133], v[26:27], v[28:29] neg_lo:[0,0,1] neg_hi:[0,0,1]
	v_pk_fma_f32 v[26:27], v[132:133], v[26:27], v[28:29] op_sel_hi:[1,0,1]
	global_store_dword v[32:33], v0, off offset:3328
	v_mov_b32_e32 v31, v27
	v_pk_add_f32 v[24:25], v[24:25], v[30:31]
	v_add_co_u32_e32 v26, vcc, s0, v134
	v_pk_mul_f32 v[28:29], v[132:133], v[24:25] op_sel:[1,1] op_sel_hi:[0,1]
	v_cvt_pk_bf16_f32 v0, v24, v25
	v_pk_fma_f32 v[30:31], v[132:133], v[24:25], v[28:29] neg_lo:[0,0,1] neg_hi:[0,0,1]
	v_pk_fma_f32 v[24:25], v[132:133], v[24:25], v[28:29] op_sel_hi:[1,0,1]
	v_addc_co_u32_e32 v27, vcc, 0, v135, vcc
	v_mov_b32_e32 v31, v25
	v_pk_add_f32 v[22:23], v[22:23], v[30:31]
	global_store_dword v[26:27], v0, off offset:512
	v_pk_mul_f32 v[24:25], v[132:133], v[22:23] op_sel:[1,1] op_sel_hi:[0,1]
	v_cvt_pk_bf16_f32 v0, v22, v23
	v_pk_fma_f32 v[28:29], v[132:133], v[22:23], v[24:25] neg_lo:[0,0,1] neg_hi:[0,0,1]
	v_pk_fma_f32 v[22:23], v[132:133], v[22:23], v[24:25] op_sel_hi:[1,0,1]
	global_store_dword v[26:27], v0, off offset:1792
	v_mov_b32_e32 v29, v23
	v_pk_add_f32 v[20:21], v[20:21], v[28:29]
	s_mov_b32 s0, 0x28212000
	v_pk_mul_f32 v[22:23], v[132:133], v[20:21] op_sel:[1,1] op_sel_hi:[0,1]
	v_cvt_pk_bf16_f32 v0, v20, v21
	v_pk_fma_f32 v[24:25], v[132:133], v[20:21], v[22:23] neg_lo:[0,0,1] neg_hi:[0,0,1]
	v_pk_fma_f32 v[20:21], v[132:133], v[20:21], v[22:23] op_sel_hi:[1,0,1]
	global_store_dword v[26:27], v0, off offset:3072
	v_mov_b32_e32 v25, v21
	v_pk_add_f32 v[18:19], v[18:19], v[24:25]
	v_add_co_u32_e32 v20, vcc, s0, v134
	v_pk_mul_f32 v[22:23], v[132:133], v[18:19] op_sel:[1,1] op_sel_hi:[0,1]
	v_cvt_pk_bf16_f32 v0, v18, v19
	v_pk_fma_f32 v[24:25], v[132:133], v[18:19], v[22:23] neg_lo:[0,0,1] neg_hi:[0,0,1]
	v_pk_fma_f32 v[18:19], v[132:133], v[18:19], v[22:23] op_sel_hi:[1,0,1]
	v_addc_co_u32_e32 v21, vcc, 0, v135, vcc
	v_mov_b32_e32 v25, v19
	v_pk_add_f32 v[16:17], v[16:17], v[24:25]
	global_store_dword v[20:21], v0, off offset:256
	v_pk_mul_f32 v[18:19], v[132:133], v[16:17] op_sel:[1,1] op_sel_hi:[0,1]
	v_cvt_pk_bf16_f32 v0, v16, v17
	v_pk_fma_f32 v[22:23], v[132:133], v[16:17], v[18:19] neg_lo:[0,0,1] neg_hi:[0,0,1]
	v_pk_fma_f32 v[16:17], v[132:133], v[16:17], v[18:19] op_sel_hi:[1,0,1]
	global_store_dword v[20:21], v0, off offset:1536
	v_mov_b32_e32 v23, v17
	s_waitcnt vmcnt(62)
; DI unsigned pk2(float lo, float hi) { f32x2 v = {lo, hi}; bf16x2v r = __builtin_convertvector(v, bf16x2v); return __builtin_bit_cast(unsigned, r); }
; DI void phase_scan(Frame& F, int l) {
;     ...
;     for (int u = F.bid; u < NG * 2; u += F.G) { const int g = u >> 1, b = (u & 1) * 8 + (F.tid >> 6), p = F.tid & 63;
;         const float lr = l32[(g * SP + p) * 2], li = l32[(g * SP + p) * 2 + 1];
;         const size_t row0 = (size_t)g * CROWS + b * NCH; float sr = 0.f, si = 0.f;
;         f32x2 ev[NCH];
; #pragma unroll
;         for (int k = 0; k < NCH; ++k) ev[k] = *(const f32x2*)(E + (row0 + k) * 128 + 2 * p);
;         asm volatile("" ::: "memory");
; #pragma unroll
;         for (int k = 0; k < NCH; ++k) {
;             *(unsigned*)(ua + (row0 + k) * UAK + 512 + 2 * p) = pk2(sr, si);
;             const float nr = lr * sr - li * si + ev[k][0], ni = lr * si + li * sr + ev[k][1]; sr = nr; si = ni; }
;     }
	v_pk_add_f32 v[14:15], v[14:15], v[22:23]
	s_mov_b32 s0, 0x28213000
	v_pk_mul_f32 v[16:17], v[132:133], v[14:15] op_sel:[1,1] op_sel_hi:[0,1]
	v_cvt_pk_bf16_f32 v0, v14, v15
	v_pk_fma_f32 v[18:19], v[132:133], v[14:15], v[16:17] neg_lo:[0,0,1] neg_hi:[0,0,1]
	v_pk_fma_f32 v[14:15], v[132:133], v[14:15], v[16:17] op_sel_hi:[1,0,1]
	global_store_dword v[20:21], v0, off offset:2816
	v_mov_b32_e32 v19, v15
	v_pk_add_f32 v[12:13], v[12:13], v[18:19]
	v_add_co_u32_e32 v14, vcc, s0, v134
	v_pk_mul_f32 v[16:17], v[132:133], v[12:13] op_sel:[1,1] op_sel_hi:[0,1]
	v_cvt_pk_bf16_f32 v0, v12, v13
	v_pk_fma_f32 v[18:19], v[132:133], v[12:13], v[16:17] neg_lo:[0,0,1] neg_hi:[0,0,1]
	v_pk_fma_f32 v[12:13], v[132:133], v[12:13], v[16:17] op_sel_hi:[1,0,1]
	v_addc_co_u32_e32 v15, vcc, 0, v135, vcc
	v_mov_b32_e32 v19, v13
	s_waitcnt vmcnt(62)
	v_pk_add_f32 v[10:11], v[10:11], v[18:19]
	global_store_dword v[14:15], v0, off
	v_pk_mul_f32 v[12:13], v[132:133], v[10:11] op_sel:[1,1] op_sel_hi:[0,1]
	v_cvt_pk_bf16_f32 v0, v10, v11
	v_pk_fma_f32 v[16:17], v[132:133], v[10:11], v[12:13] neg_lo:[0,0,1] neg_hi:[0,0,1]
	v_pk_fma_f32 v[10:11], v[132:133], v[10:11], v[12:13] op_sel_hi:[1,0,1]
	global_store_dword v[14:15], v0, off offset:1280
	v_mov_b32_e32 v17, v11
	s_waitcnt vmcnt(62)
	v_pk_add_f32 v[8:9], v[8:9], v[16:17]
	s_nop 0
	v_pk_mul_f32 v[10:11], v[132:133], v[8:9] op_sel:[1,1] op_sel_hi:[0,1]
	v_cvt_pk_bf16_f32 v0, v8, v9
	v_pk_fma_f32 v[12:13], v[132:133], v[8:9], v[10:11] neg_lo:[0,0,1] neg_hi:[0,0,1]
	v_pk_fma_f32 v[8:9], v[132:133], v[8:9], v[10:11] op_sel_hi:[1,0,1]
	global_store_dword v[14:15], v0, off offset:2560
	v_mov_b32_e32 v13, v9
	v_pk_add_f32 v[6:7], v[6:7], v[12:13]
	s_nop 0
	v_cvt_pk_bf16_f32 v0, v6, v7
	global_store_dword v[14:15], v0, off offset:3840
	s_cbranch_scc1 .LBB0_397

; DI const float* inp(kptr_t k, int i) { return (const float*)k[i]; }
; DI void refresh(Frame& F) { int w = F.wave; unsigned ones_ = ~0u; asm volatile("" : "+s"(w), "+s"(ones_)); int ln = (int)__builtin_amdgcn_mbcnt_hi(ones_, __builtin_amdgcn_mbcnt_lo(ones_, 0u)); asm volatile("" : "+v"(ln)); F.tid = w * 64 + ln; F.lane = ln; F.wave = w; int b = blockIdx.x; asm volatile("" : "+s"(b)); F.bid = b; }
; DI void phase_attn(Frame& F, int l) {
;     ...
;     for (int U = F.bid; U < NB * NH * NBLK; U += F.G) {
;         refresh(F);
;         const int lane = F.lane, wave = F.wave, qi = lane & 31, hh = lane >> 5;
;         const int srow = F.tid >> 3, sch = F.tid & 7;
;         const int c = U & 255, it = U >> 8, bh = c >> 1, set = c & 1;
;         const int qblk = set ? (it == 0 ? 6 : (it == 1 ? 1 : (it == 2 ? 5 : 2))) : (it == 0 ? 7 : (it == 1 ? 0 : (it == 2 ? 4 : 3)));
;         const int b = bh >> 3, h = bh & 7;
;         const size_t qtok = (size_t)b * SEQ + qblk * 256 + 32 * wave + qi;
;         bf16x8 qf[4];
; #pragma unroll
;         for (int s = 0; s < 4; ++s) qf[s] = *(const bf16x8*)(qb + qtok * AW + h * HD + 16 * s + 8 * hh);
;         u32x4 kreg, vreg;
;         { const size_t tok = (size_t)b * SEQ + qblk * 256 + srow; kreg = *(const u32x4*)(kb + tok * AW + h * HD + sch * 8); vreg = *(const u32x4*)(vb + tok * AW + h * HD + sch * 8); }
;         const float km_v = kmean[((size_t)(b * NBLK + (F.tid >> 6))) * AW + h * HD + (F.tid & 63)] * (1.0f / 256.0f);
;         const float bias_v = inp(KA, I_RELB)[t5_bucket(F.tid & 127) * NH + h] * LOG2E;
.LBB0_479:
	s_bfe_u32 s4, s51, 0x40004
	s_lshl_b32 s16, s4, 11
	s_lshl_b32 s2, s37, 8
	s_lshl_b32 s36, s97, 5
	s_lshl_b32 s0, s97, 6
	s_bfe_u32 s1, s51, 0x30001
	s_add_i32 s58, s2, s16
	s_ashr_i32 s2, s36, 31
	s_add_u32 s3, s58, s36
	v_and_b32_e32 v188, 31, v186
	s_addc_u32 s2, 0, s2
	s_waitcnt vmcnt(0)
	v_or_b32_e32 v2, s3, v188
	v_mov_b32_e32 v3, s2
	v_readlane_b32 s2, v253, 19
	v_ashrrev_i32_e32 v16, 5, v186
	v_lshlrev_b64 v[170:171], 10, v[2:3]
	v_readlane_b32 s3, v253, 20
	v_add_u32_e32 v17, s0, v186
	v_lshlrev_b32_e32 v168, 3, v16
	v_lshl_add_u64 v[2:3], s[2:3], 0, v[170:171]
	s_lshl_b32 s2, s1, 7
	s_mov_b32 s3, s59
	v_ashrrev_i32_e32 v10, 3, v17
	v_lshl_add_u64 v[2:3], v[2:3], 0, s[2:3]
	v_ashrrev_i32_e32 v169, 31, v168
	v_lshl_add_u64 v[2:3], v[168:169], 1, v[2:3]
	v_ashrrev_i32_e32 v11, 31, v10
	v_ashrrev_i32_e32 v19, 6, v17
	global_load_dwordx4 v[156:159], v[2:3], off nt
	global_load_dwordx4 v[152:155], v[2:3], off offset:32 nt
	global_load_dwordx4 v[148:151], v[2:3], off offset:64 nt
	global_load_dwordx4 v[144:147], v[2:3], off offset:96 nt
	v_lshl_add_u64 v[2:3], s[58:59], 0, v[10:11]
	v_readlane_b32 s8, v253, 31
	v_lshl_add_u32 v20, s4, 3, v19
	v_lshlrev_b64 v[2:3], 10, v[2:3]
	v_readlane_b32 s9, v253, 32
	v_ashrrev_i32_e32 v21, 31, v20
	v_and_b32_e32 v19, 63, v186
	v_lshl_add_u64 v[14:15], s[8:9], 0, v[2:3]
	v_readlane_b32 s8, v253, 15
	v_lshlrev_b64 v[20:21], 11, v[20:21]
	v_and_b32_e32 v18, 7, v186
	v_readlane_b32 s9, v253, 16
	v_lshl_add_u64 v[20:21], s[34:35], 0, v[20:21]
	v_lshlrev_b32_e32 v22, 2, v19
	v_mov_b32_e32 v23, v1
	v_lshl_add_u64 v[4:5], v[14:15], 0, s[2:3]
	v_lshlrev_b32_e32 v0, 4, v18
	v_lshl_add_u64 v[12:13], s[8:9], 0, v[2:3]
	v_lshl_add_u64 v[20:21], v[20:21], 0, v[22:23]
	s_lshl_b32 s58, s1, 8
	v_lshl_add_u64 v[178:179], v[4:5], 0, v[0:1]
	v_lshl_add_u64 v[2:3], v[12:13], 0, s[2:3]
	v_lshl_add_u64 v[20:21], v[20:21], 0, s[58:59]
	v_lshl_add_u64 v[180:181], v[2:3], 0, v[0:1]
	global_load_dwordx4 v[2:5], v[178:179], off
	global_load_dwordx4 v[6:9], v[180:181], off
	global_load_dword v19, v[20:21], off
	v_and_b32_e32 v20, 0x7f, v17
	v_cmp_lt_u32_e32 vcc, 15, v20
	s_and_saveexec_b64 s[2:3], vcc
	s_cbranch_execz .LBB0_481
	v_cmp_lt_u32_e32 vcc, 18, v20
	s_movk_i32 s4, 0x42
	s_nop 0
	v_cndmask_b32_e64 v21, 16, 17, vcc
	v_cmp_lt_u32_e32 vcc, 20, v20
	s_nop 1
	v_cndmask_b32_e64 v22, 0, 1, vcc
	v_cmp_lt_u32_e32 vcc, 23, v20
	s_nop 1
	v_addc_co_u32_e32 v21, vcc, v21, v22, vcc
	v_cmp_lt_u32_e32 vcc, 26, v20
	s_nop 1
	v_cndmask_b32_e64 v22, 0, 1, vcc
	v_cmp_lt_u32_e32 vcc, 30, v20
	s_nop 1
	v_addc_co_u32_e32 v21, vcc, v21, v22, vcc
	v_cmp_lt_u32_e32 vcc, 34, v20
	s_nop 1
	v_cndmask_b32_e64 v22, 0, 1, vcc
	v_cmp_lt_u32_e32 vcc, 39, v20
	s_nop 1
	v_addc_co_u32_e32 v21, vcc, v21, v22, vcc
	v_cmp_lt_u32_e32 vcc, 45, v20
	s_nop 1
	v_cndmask_b32_e64 v22, 0, 1, vcc
	v_cmp_lt_u32_e32 vcc, 51, v20
	s_nop 1
	v_addc_co_u32_e32 v21, vcc, v21, v22, vcc
	v_cmp_lt_u32_e32 vcc, 58, v20
	s_nop 1
	v_cndmask_b32_e64 v22, 0, 1, vcc
	v_cmp_lt_u32_e32 vcc, s4, v20
	s_movk_i32 s4, 0x4c
	s_nop 0
	v_addc_co_u32_e32 v21, vcc, v21, v22, vcc
	v_cmp_lt_u32_e32 vcc, s4, v20
	s_movk_i32 s4, 0x56
	s_nop 0
	v_cndmask_b32_e64 v22, 0, 1, vcc
	v_cmp_lt_u32_e32 vcc, s4, v20
	s_movk_i32 s4, 0x62
	s_nop 0
	v_addc_co_u32_e32 v21, vcc, v21, v22, vcc
	v_cmp_lt_u32_e32 vcc, s4, v20
	s_movk_i32 s4, 0x70
	s_nop 0
	v_cndmask_b32_e64 v22, 0, 1, vcc
	v_cmp_lt_u32_e32 vcc, s4, v20
	s_nop 1
	v_addc_co_u32_e32 v20, vcc, v21, v22, vcc
